# speedup vs baseline: 1.0381x; 1.0381x over previous
_Z6k_prepPKiS0_PiS1_S1_S1_S1_S1_S1_PKfPKDF16_PDF16_Pf:
	s_cmpk_lt_u32 s2, 521
	s_cbranch_scc1 .Lp1_entry
	s_cmpk_lt_u32 s2, 717
	s_cbranch_scc1 .Lp2_entry
	s_cmpk_lt_u32 s2, 2280
	s_cbranch_scc1 .Lpx_entry
	s_endpgm
.Lpx_entry:
	v_and_b32_e32 v50, 63, v0
	s_load_dwordx2 s[4:5], s[0:1], 0x50
	v_lshlrev_b32_e32 v1, 4, v0
	v_or_b32_e32 v18, 0x80, v0
	v_lshlrev_b32_e32 v10, 4, v18
	v_or_b32_e32 v20, 0x180, v0
	s_waitcnt lgkmcnt(0)
	global_load_dwordx4 v[2:5], v1, s[4:5]
	global_load_dwordx4 v[6:9], v10, s[4:5]
	v_or_b32_e32 v1, 0x100, v0
	v_lshlrev_b32_e32 v19, 4, v1
	v_lshlrev_b32_e32 v21, 4, v20
	global_load_dwordx4 v[10:13], v19, s[4:5]
	global_load_dwordx4 v[14:17], v21, s[4:5]
	v_lshrrev_b32_e32 v19, 4, v0
	s_sub_i32 s8, s2, 0x2cd
	s_lshl_b32 s8, s8, 1
	v_lshrrev_b32_e32 v23, 6, v0
	s_movk_i32 s4, 0x70
	s_movk_i32 s5, 0xf0
	v_mov_b32_e32 v21, 0x80
	s_movk_i32 s6, 0x170
	s_movk_i32 s7, 0x1f0
	v_mov_b32_e32 v22, 0x180
	v_bitop3_b32 v19, v19, 15, v0 bitop3:0x48
	v_lshrrev_b32_e32 v18, 4, v18
	v_lshrrev_b32_e32 v20, 4, v20
	v_or_b32_e32 v23, s8, v23
	s_mov_b32 s3, 0xc350
	v_bitop3_b32 v21, v0, s5, v21 bitop3:0xc8
	v_bitop3_b32 v22, v0, s7, v22 bitop3:0xc8
	v_and_or_b32 v24, v0, s4, v19
	v_xor_b32_e32 v18, v18, v0
	v_and_or_b32 v19, v1, s6, v19
	v_xor_b32_e32 v20, v20, v0
	v_lshlrev_b32_e32 v1, 4, v23
	v_lshlrev_b32_e32 v23, 4, v24
	v_and_or_b32 v18, v18, 15, v21
	v_and_or_b32 v20, v20, 15, v22
	v_cmp_gt_i32_e32 vcc, s3, v1
	v_lshlrev_b32_e32 v19, 4, v19
	v_lshlrev_b32_e32 v18, 4, v18
	v_lshlrev_b32_e32 v20, 4, v20
	s_waitcnt vmcnt(3)
	ds_write_b128 v23, v[2:5]
	s_waitcnt vmcnt(2)
	ds_write_b128 v18, v[6:9]
	s_waitcnt vmcnt(1)
	ds_write_b128 v19, v[10:13]
	s_waitcnt vmcnt(0)
	ds_write_b128 v20, v[14:17]
	s_waitcnt lgkmcnt(0)
	s_barrier
	s_and_saveexec_b64 s[6:7], vcc
	s_cbranch_execz .LBB1_12
	v_and_b32_e32 v51, 15, v0
	s_load_dwordx2 s[4:5], s[0:1], 0x48
	v_or_b32_e32 v46, v1, v51
	v_mov_b32_e32 v2, 0xc34f
	v_cmp_gt_i32_e32 vcc, s3, v46
	v_lshrrev_b32_e32 v1, 4, v50
	v_lshlrev_b32_e32 v42, 5, v1
	v_cndmask_b32_e32 v2, v2, v46, vcc
	v_ashrrev_i32_e32 v3, 31, v2
	v_lshlrev_b64 v[2:3], 9, v[2:3]
	s_waitcnt lgkmcnt(0)
	v_lshl_add_u64 v[2:3], s[4:5], 0, v[2:3]
	v_mov_b32_e32 v43, 0
	v_lshl_add_u64 v[30:31], v[2:3], 0, v[42:43]
	global_load_dwordx4 v[26:29], v[30:31], off offset:16 nt
	global_load_dwordx4 v[34:37], v[30:31], off nt
	global_load_dwordx4 v[18:21], v[30:31], off offset:144 nt
	global_load_dwordx4 v[22:25], v[30:31], off offset:128 nt
	global_load_dwordx4 v[10:13], v[30:31], off offset:272 nt
	global_load_dwordx4 v[14:17], v[30:31], off offset:256 nt
	global_load_dwordx4 v[2:5], v[30:31], off offset:400 nt
	global_load_dwordx4 v[6:9], v[30:31], off offset:384 nt
	s_load_dwordx2 s[4:5], s[0:1], 0x58
	v_bitop3_b32 v30, v1, v0, 15 bitop3:0x78
	v_lshlrev_b32_e32 v31, 8, v51
	v_lshl_or_b32 v38, v30, 4, v31
	ds_read_b128 v[30:33], v38
	ds_read_b128 v[38:41], v38 offset:4096
	v_ashrrev_i32_e32 v47, 31, v46
	v_lshlrev_b64 v[44:45], 8, v[46:47]
	s_waitcnt lgkmcnt(0)
	v_lshl_add_u64 v[44:45], s[4:5], 0, v[44:45]
	v_and_b32_e32 v42, 48, v50
	v_lshlrev_b32_e32 v52, 7, v51
	v_lshl_add_u64 v[48:49], v[44:45], 0, v[42:43]
	s_waitcnt vmcnt(7)
	v_cvt_pk_f16_f32 v44, v26, v27
	s_waitcnt vmcnt(6)
	v_cvt_f16_f32_e32 v54, v34
	v_cvt_f16_f32_e32 v53, v35
	v_cvt_pk_f16_f32 v42, v34, v35
	v_cvt_pk_f16_f32 v43, v36, v37
	v_cvt_pk_f16_f32 v45, v28, v29
	s_and_saveexec_b64 s[4:5], vcc
	s_cbranch_execz .LBB1_4
	global_store_dwordx4 v[48:49], v[42:45], off

.LBB1_10:
	s_or_b64 exec, exec, s[4:5]
	v_cvt_f32_f16_e32 v24, v23
	v_cvt_f32_f16_e32 v25, v22
	v_cvt_f32_f16_sdwa v23, v19 dst_sel:DWORD dst_unused:UNUSED_PAD src0_sel:WORD_1
	v_cvt_f32_f16_e32 v22, v19
	v_sub_f32_e32 v6, v6, v24
	v_sub_f32_e32 v7, v7, v25
	s_waitcnt lgkmcnt(1)
	v_mfma_f32_16x16x32_f16 a[0:3], v[10:13], v[18:21], a[0:3]
	v_add_f32_e64 v8, v8, -v22
	v_add_f32_e64 v9, v9, -v23
	v_cvt_pk_f16_f32 v6, v6, v7
	v_cvt_pk_f16_f32 v7, v8, v9
	v_cvt_f32_f16_sdwa v9, v20 dst_sel:DWORD dst_unused:UNUSED_PAD src0_sel:WORD_1
	v_cvt_f32_f16_e32 v8, v20
	v_cvt_f32_f16_sdwa v23, v21 dst_sel:DWORD dst_unused:UNUSED_PAD src0_sel:WORD_1
	v_cvt_f32_f16_e32 v22, v21
	s_waitcnt lgkmcnt(0)
	v_mfma_f32_16x16x32_f16 a[0:3], v[14:17], v[18:21], a[0:3]
	v_add_f32_e64 v2, v2, -v8
	v_add_f32_e64 v3, v3, -v9
	v_cmp_gt_u32_e64 s[4:5], 32, v50
	v_cvt_pk_f16_f32 v8, v2, v3
	v_pk_add_f32 v[2:3], v[4:5], v[22:23] neg_lo:[0,1] neg_hi:[0,1]
	s_and_b64 s[4:5], s[4:5], vcc
	v_cvt_pk_f16_f32 v9, v2, v3
	s_nop 1
	v_mfma_f32_16x16x32_f16 a[0:3], v[10:13], v[6:9], a[0:3]
	s_and_b64 exec, exec, s[4:5]
	s_cbranch_execz .LBB1_12
	s_load_dwordx2 s[4:5], s[0:1], 0x60
	s_nop 4
	v_accvgpr_read_b32 v5, a3
	v_lshlrev_b64 v[6:7], 5, v[46:47]
	v_accvgpr_read_b32 v4, a2
	v_accvgpr_read_b32 v3, a1
	v_accvgpr_read_b32 v2, a0
	v_lshlrev_b32_e32 v8, 4, v1
	v_mov_b32_e32 v9, 0
	s_waitcnt lgkmcnt(0)
	v_lshl_add_u64 v[6:7], s[4:5], 0, v[6:7]
	s_mov_b32 s4, 0x3fb8aa3b
	v_lshl_add_u64 v[6:7], v[6:7], 0, v[8:9]
	v_pk_mul_f32 v[2:3], v[2:3], s[4:5] op_sel_hi:[1,0]
	v_pk_mul_f32 v[4:5], v[4:5], s[4:5] op_sel_hi:[1,0]
	global_store_dwordx4 v[6:7], v[2:5], off
.LBB1_12:
	s_endpgm
.Lp1_entry:
	s_load_dwordx4 s[4:7], s[0:1], 0x0
	s_load_dwordx2 s[8:9], s[0:1], 0x20
	s_load_dwordx2 s[10:11], s[0:1], 0x28
	s_load_dwordx2 s[12:13], s[0:1], 0x50
	v_lshlrev_b32_e32 v1, 3, v0
	v_mov_b32_e32 v2, 0
	v_mov_b32_e32 v3, 0
	ds_write_b64 v1, v[2:3]
	s_mul_i32 s3, s2, 0x180
	v_add_u32_e32 v4, s3, v0
	v_add_u32_e32 v5, 0x80, v4
	v_add_u32_e32 v6, 0x100, v4
	s_mov_b32 s14, 0x30d40
	v_cmp_gt_u32_e64 s[16:17], s14, v4
	v_cmp_gt_u32_e64 s[18:19], s14, v5
	v_cmp_gt_u32_e64 s[20:21], s14, v6
	v_min_u32_e32 v4, 0x30d3f, v4
	v_min_u32_e32 v5, 0x30d3f, v5
	v_min_u32_e32 v6, 0x30d3f, v6
	v_lshlrev_b32_e32 v4, 4, v4
	v_lshlrev_b32_e32 v5, 4, v5
	v_lshlrev_b32_e32 v6, 4, v6
	s_waitcnt lgkmcnt(0)
	s_add_u32 s14, s4, 0x30d400
	s_addc_u32 s15, s5, 0
	global_load_dwordx4 v[8:11], v4, s[6:7] nt
	global_load_dwordx4 v[12:15], v4, s[4:5] nt
	global_load_dwordx4 v[16:19], v4, s[14:15] nt
	global_load_dwordx4 v[20:23], v5, s[6:7] nt
	global_load_dwordx4 v[24:27], v5, s[4:5] nt
	global_load_dwordx4 v[28:31], v5, s[14:15] nt
	global_load_dwordx4 v[32:35], v6, s[6:7] nt
	global_load_dwordx4 v[36:39], v6, s[4:5] nt
	global_load_dwordx4 v[40:43], v6, s[14:15] nt
	v_mov_b32_e32 v48, 1
	s_mov_b32 s31, 0
	s_mov_b32 s30, 0xc350
	s_barrier
	s_waitcnt vmcnt(6)
	v_mul_lo_u32 v44, v12, v8
	v_mul_lo_u32 v45, v16, v8
	v_cmp_ne_u32_e64 s[22:23], 0, v8
	v_max_u32_e32 v46, v44, v45
	v_cmp_gt_u32_e32 vcc, s30, v46
	s_and_b64 vcc, vcc, s[22:23]
	s_and_b64 vcc, vcc, s[16:17]
	s_andn2_b64 s[24:25], s[16:17], s[22:23]
	s_bcnt1_i32_b64 s26, s[24:25]
	s_add_i32 s31, s31, s26
	v_lshl_or_b32 v12, v45, 16, v44
	v_cndmask_b32_e32 v12, -1, v12, vcc
	v_lshrrev_b32_e32 v47, 22, v12
	v_and_b32_e32 v47, 0x3fc, v47
	ds_add_rtn_u32 v16, v47, v48
	v_mul_lo_u32 v44, v13, v9
	v_mul_lo_u32 v45, v17, v9
	v_cmp_ne_u32_e64 s[22:23], 0, v9
	v_max_u32_e32 v46, v44, v45
	v_cmp_gt_u32_e32 vcc, s30, v46
	s_and_b64 vcc, vcc, s[22:23]
	s_and_b64 vcc, vcc, s[16:17]
	s_andn2_b64 s[24:25], s[16:17], s[22:23]
	s_bcnt1_i32_b64 s26, s[24:25]
	s_add_i32 s31, s31, s26
	v_lshl_or_b32 v13, v45, 16, v44
	v_cndmask_b32_e32 v13, -1, v13, vcc
	v_lshrrev_b32_e32 v47, 22, v13
	v_and_b32_e32 v47, 0x3fc, v47
	ds_add_rtn_u32 v17, v47, v48
	v_mul_lo_u32 v44, v14, v10
	v_mul_lo_u32 v45, v18, v10
	v_cmp_ne_u32_e64 s[22:23], 0, v10
	v_max_u32_e32 v46, v44, v45
	v_cmp_gt_u32_e32 vcc, s30, v46
	s_and_b64 vcc, vcc, s[22:23]
	s_and_b64 vcc, vcc, s[16:17]
	s_andn2_b64 s[24:25], s[16:17], s[22:23]
	s_bcnt1_i32_b64 s26, s[24:25]
	s_add_i32 s31, s31, s26
	v_lshl_or_b32 v14, v45, 16, v44
	v_cndmask_b32_e32 v14, -1, v14, vcc
	v_lshrrev_b32_e32 v47, 22, v14
	v_and_b32_e32 v47, 0x3fc, v47
	ds_add_rtn_u32 v18, v47, v48
	v_mul_lo_u32 v44, v15, v11
	v_mul_lo_u32 v45, v19, v11
	v_cmp_ne_u32_e64 s[22:23], 0, v11
	v_max_u32_e32 v46, v44, v45
	v_cmp_gt_u32_e32 vcc, s30, v46
	s_and_b64 vcc, vcc, s[22:23]
	s_and_b64 vcc, vcc, s[16:17]
	s_andn2_b64 s[24:25], s[16:17], s[22:23]
	s_bcnt1_i32_b64 s26, s[24:25]
	s_add_i32 s31, s31, s26
	v_lshl_or_b32 v15, v45, 16, v44
	v_cndmask_b32_e32 v15, -1, v15, vcc
	v_lshrrev_b32_e32 v47, 22, v15
	v_and_b32_e32 v47, 0x3fc, v47
	ds_add_rtn_u32 v19, v47, v48
	s_waitcnt vmcnt(3)
	v_mul_lo_u32 v44, v24, v20
	v_mul_lo_u32 v45, v28, v20
	v_cmp_ne_u32_e64 s[22:23], 0, v20
	v_max_u32_e32 v46, v44, v45
	v_cmp_gt_u32_e32 vcc, s30, v46
	s_and_b64 vcc, vcc, s[22:23]
	s_and_b64 vcc, vcc, s[18:19]
	s_andn2_b64 s[24:25], s[18:19], s[22:23]
	s_bcnt1_i32_b64 s26, s[24:25]
	s_add_i32 s31, s31, s26
	v_lshl_or_b32 v24, v45, 16, v44
	v_cndmask_b32_e32 v24, -1, v24, vcc
	v_lshrrev_b32_e32 v47, 22, v24
	v_and_b32_e32 v47, 0x3fc, v47
	ds_add_rtn_u32 v28, v47, v48
	v_mul_lo_u32 v44, v25, v21
	v_mul_lo_u32 v45, v29, v21
	v_cmp_ne_u32_e64 s[22:23], 0, v21
	v_max_u32_e32 v46, v44, v45
	v_cmp_gt_u32_e32 vcc, s30, v46
	s_and_b64 vcc, vcc, s[22:23]
	s_and_b64 vcc, vcc, s[18:19]
	s_andn2_b64 s[24:25], s[18:19], s[22:23]
	s_bcnt1_i32_b64 s26, s[24:25]
	s_add_i32 s31, s31, s26
	v_lshl_or_b32 v25, v45, 16, v44
	v_cndmask_b32_e32 v25, -1, v25, vcc
	v_lshrrev_b32_e32 v47, 22, v25
	v_and_b32_e32 v47, 0x3fc, v47
	ds_add_rtn_u32 v29, v47, v48
	v_mul_lo_u32 v44, v26, v22
	v_mul_lo_u32 v45, v30, v22
	v_cmp_ne_u32_e64 s[22:23], 0, v22
	v_max_u32_e32 v46, v44, v45
	v_cmp_gt_u32_e32 vcc, s30, v46
	s_and_b64 vcc, vcc, s[22:23]
	s_and_b64 vcc, vcc, s[18:19]
	s_andn2_b64 s[24:25], s[18:19], s[22:23]
	s_bcnt1_i32_b64 s26, s[24:25]
	s_add_i32 s31, s31, s26
	v_lshl_or_b32 v26, v45, 16, v44
	v_cndmask_b32_e32 v26, -1, v26, vcc
	v_lshrrev_b32_e32 v47, 22, v26
	v_and_b32_e32 v47, 0x3fc, v47
	ds_add_rtn_u32 v30, v47, v48
	v_mul_lo_u32 v44, v27, v23
	v_mul_lo_u32 v45, v31, v23
	v_cmp_ne_u32_e64 s[22:23], 0, v23
	v_max_u32_e32 v46, v44, v45
	v_cmp_gt_u32_e32 vcc, s30, v46
	s_and_b64 vcc, vcc, s[22:23]
	s_and_b64 vcc, vcc, s[18:19]
	s_andn2_b64 s[24:25], s[18:19], s[22:23]
	s_bcnt1_i32_b64 s26, s[24:25]
	s_add_i32 s31, s31, s26
	v_lshl_or_b32 v27, v45, 16, v44
	v_cndmask_b32_e32 v27, -1, v27, vcc
	v_lshrrev_b32_e32 v47, 22, v27
	v_and_b32_e32 v47, 0x3fc, v47
	ds_add_rtn_u32 v31, v47, v48
	s_waitcnt vmcnt(0)
	v_mul_lo_u32 v44, v36, v32
	v_mul_lo_u32 v45, v40, v32
	v_cmp_ne_u32_e64 s[22:23], 0, v32
	v_max_u32_e32 v46, v44, v45
	v_cmp_gt_u32_e32 vcc, s30, v46
	s_and_b64 vcc, vcc, s[22:23]
	s_and_b64 vcc, vcc, s[20:21]
	s_andn2_b64 s[24:25], s[20:21], s[22:23]
	s_bcnt1_i32_b64 s26, s[24:25]
	s_add_i32 s31, s31, s26
	v_lshl_or_b32 v36, v45, 16, v44
	v_cndmask_b32_e32 v36, -1, v36, vcc
	v_lshrrev_b32_e32 v47, 22, v36
	v_and_b32_e32 v47, 0x3fc, v47
	ds_add_rtn_u32 v40, v47, v48
	v_mul_lo_u32 v44, v37, v33
	v_mul_lo_u32 v45, v41, v33
	v_cmp_ne_u32_e64 s[22:23], 0, v33
	v_max_u32_e32 v46, v44, v45
	v_cmp_gt_u32_e32 vcc, s30, v46
	s_and_b64 vcc, vcc, s[22:23]
	s_and_b64 vcc, vcc, s[20:21]
	s_andn2_b64 s[24:25], s[20:21], s[22:23]
	s_bcnt1_i32_b64 s26, s[24:25]
	s_add_i32 s31, s31, s26
	v_lshl_or_b32 v37, v45, 16, v44
	v_cndmask_b32_e32 v37, -1, v37, vcc
	v_lshrrev_b32_e32 v47, 22, v37
	v_and_b32_e32 v47, 0x3fc, v47
	ds_add_rtn_u32 v41, v47, v48
	v_mul_lo_u32 v44, v38, v34
	v_mul_lo_u32 v45, v42, v34
	v_cmp_ne_u32_e64 s[22:23], 0, v34
	v_max_u32_e32 v46, v44, v45
	v_cmp_gt_u32_e32 vcc, s30, v46
	s_and_b64 vcc, vcc, s[22:23]
	s_and_b64 vcc, vcc, s[20:21]
	s_andn2_b64 s[24:25], s[20:21], s[22:23]
	s_bcnt1_i32_b64 s26, s[24:25]
	s_add_i32 s31, s31, s26
	v_lshl_or_b32 v38, v45, 16, v44
	v_cndmask_b32_e32 v38, -1, v38, vcc
	v_lshrrev_b32_e32 v47, 22, v38
	v_and_b32_e32 v47, 0x3fc, v47
	ds_add_rtn_u32 v42, v47, v48
	v_mul_lo_u32 v44, v39, v35
	v_mul_lo_u32 v45, v43, v35
	v_cmp_ne_u32_e64 s[22:23], 0, v35
	v_max_u32_e32 v46, v44, v45
	v_cmp_gt_u32_e32 vcc, s30, v46
	s_and_b64 vcc, vcc, s[22:23]
	s_and_b64 vcc, vcc, s[20:21]
	s_andn2_b64 s[24:25], s[20:21], s[22:23]
	s_bcnt1_i32_b64 s26, s[24:25]
	s_add_i32 s31, s31, s26
	v_lshl_or_b32 v39, v45, 16, v44
	v_cndmask_b32_e32 v39, -1, v39, vcc
	v_lshrrev_b32_e32 v47, 22, v39
	v_and_b32_e32 v47, 0x3fc, v47
	ds_add_rtn_u32 v43, v47, v48
	s_waitcnt lgkmcnt(0)
	s_barrier
	v_readfirstlane_b32 s3, v0
	s_cmp_lt_u32 s3, 64
	s_cbranch_scc0 .Lp1_scan_done
	v_lshlrev_b32_e32 v1, 4, v0
	ds_read_b128 v[8:11], v1
	s_waitcnt lgkmcnt(0)
	v_add_u32_e32 v20, v8, v9
	v_add_u32_e32 v21, v20, v10
	v_add_u32_e32 v22, v21, v11
	v_mov_b32_e32 v23, v22
	s_nop 1
	v_add_u32_dpp v23, v23, v23 row_shr:1 row_mask:0xf bank_mask:0xf bound_ctrl:1
	s_nop 1
	v_add_u32_dpp v23, v23, v23 row_shr:2 row_mask:0xf bank_mask:0xf bound_ctrl:1
	s_nop 1
	v_add_u32_dpp v23, v23, v23 row_shr:4 row_mask:0xf bank_mask:0xf bound_ctrl:1
	s_nop 1
	v_add_u32_dpp v23, v23, v23 row_shr:8 row_mask:0xf bank_mask:0xf bound_ctrl:1
	s_nop 1
	v_add_u32_dpp v23, v23, v23 row_bcast:15 row_mask:0xa bank_mask:0xf
	s_nop 1
	v_add_u32_dpp v23, v23, v23 row_bcast:31 row_mask:0xc bank_mask:0xf
	s_nop 1
	v_sub_u32_e32 v32, v23, v22
	v_add_u32_e32 v33, v32, v8
	v_add_u32_e32 v34, v32, v20
	v_add_u32_e32 v35, v32, v21
	ds_write_b128 v1, v[32:35]
	v_lshl_or_b32 v8, v8, 16, v32
	v_lshl_or_b32 v9, v9, 16, v33
	v_lshl_or_b32 v10, v10, 16, v34
	v_lshl_or_b32 v11, v11, 16, v35
	s_lshl_b32 s3, s2, 10
	s_add_u32 s24, s12, 0x41a000
	s_addc_u32 s25, s13, 0
	s_add_u32 s24, s24, s3
	s_addc_u32 s25, s25, 0
	global_store_dwordx4 v1, v[8:11], s[24:25] sc1
.Lp1_scan_done:
	s_waitcnt lgkmcnt(0)
	s_barrier
	v_lshrrev_b32_e32 v8, 22, v12
	v_and_b32_e32 v8, 0x3fc, v8
	v_lshrrev_b32_e32 v9, 22, v13
	v_and_b32_e32 v9, 0x3fc, v9
	v_lshrrev_b32_e32 v10, 22, v14
	v_and_b32_e32 v10, 0x3fc, v10
	v_lshrrev_b32_e32 v11, 22, v15
	v_and_b32_e32 v11, 0x3fc, v11
	v_lshrrev_b32_e32 v20, 22, v24
	v_and_b32_e32 v20, 0x3fc, v20
	v_lshrrev_b32_e32 v21, 22, v25
	v_and_b32_e32 v21, 0x3fc, v21
	v_lshrrev_b32_e32 v22, 22, v26
	v_and_b32_e32 v22, 0x3fc, v22
	v_lshrrev_b32_e32 v23, 22, v27
	v_and_b32_e32 v23, 0x3fc, v23
	v_lshrrev_b32_e32 v32, 22, v36
	v_and_b32_e32 v32, 0x3fc, v32
	v_lshrrev_b32_e32 v33, 22, v37
	v_and_b32_e32 v33, 0x3fc, v33
	v_lshrrev_b32_e32 v34, 22, v38
	v_and_b32_e32 v34, 0x3fc, v34
	v_lshrrev_b32_e32 v35, 22, v39
	v_and_b32_e32 v35, 0x3fc, v35
	ds_read_b32 v8, v8
	ds_read_b32 v9, v9
	ds_read_b32 v10, v10
	ds_read_b32 v11, v11
	ds_read_b32 v20, v20
	ds_read_b32 v21, v21
	ds_read_b32 v22, v22
	ds_read_b32 v23, v23
	ds_read_b32 v32, v32
	ds_read_b32 v33, v33
	ds_read_b32 v34, v34
	ds_read_b32 v35, v35
	s_waitcnt lgkmcnt(0)
	v_add_lshl_u32 v8, v8, v16, 2
	ds_write_b32 v8, v12 offset:1024
	v_add_lshl_u32 v9, v9, v17, 2
	ds_write_b32 v9, v13 offset:1024
	v_add_lshl_u32 v10, v10, v18, 2
	ds_write_b32 v10, v14 offset:1024
	v_add_lshl_u32 v11, v11, v19, 2
	ds_write_b32 v11, v15 offset:1024
	v_add_lshl_u32 v20, v20, v28, 2
	ds_write_b32 v20, v24 offset:1024
	v_add_lshl_u32 v21, v21, v29, 2
	ds_write_b32 v21, v25 offset:1024
	v_add_lshl_u32 v22, v22, v30, 2
	ds_write_b32 v22, v26 offset:1024
	v_add_lshl_u32 v23, v23, v31, 2
	ds_write_b32 v23, v27 offset:1024
	v_add_lshl_u32 v32, v32, v40, 2
	ds_write_b32 v32, v36 offset:1024
	v_add_lshl_u32 v33, v33, v41, 2
	ds_write_b32 v33, v37 offset:1024
	v_add_lshl_u32 v34, v34, v42, 2
	ds_write_b32 v34, v38 offset:1024
	v_add_lshl_u32 v35, v35, v43, 2
	ds_write_b32 v35, v39 offset:1024
	s_waitcnt lgkmcnt(0)
	s_barrier
	v_lshlrev_b32_e32 v1, 4, v0
	ds_read_b128 v[8:11], v1 offset:1024
	ds_read_b128 v[12:15], v1 offset:3072
	ds_read_b128 v[16:19], v1 offset:5120
	s_mul_i32 s3, s2, 0x1800
	s_add_u32 s26, s12, 0x1a000
	s_addc_u32 s27, s13, 0
	s_add_u32 s26, s26, s3
	s_addc_u32 s27, s27, 0
	v_add_u32_e32 v2, 0x1000, v1
	s_waitcnt lgkmcnt(2)
	global_store_dwordx4 v1, v[8:11], s[26:27] sc1
	s_waitcnt lgkmcnt(1)
	global_store_dwordx4 v1, v[12:15], s[26:27] offset:2048 sc1
	s_waitcnt lgkmcnt(0)
	global_store_dwordx4 v2, v[16:19], s[26:27] sc1
	s_waitcnt vmcnt(0)
	s_barrier
	v_and_b32_e32 v1, 63, v0
	v_cmp_eq_u32_e32 vcc, 0, v1
	s_and_saveexec_b64 s[22:23], vcc
	s_cbranch_execz .Lp1_end
	s_cmp_eq_u32 s31, 0
	s_cbranch_scc1 .Lp1_nomask
	s_and_b32 s3, s2, 63
	s_lshl_b32 s3, s3, 6
	v_mov_b32_e32 v2, s31
	v_mov_b32_e32 v3, s3
	global_atomic_add v3, v2, s[8:9]
.Lp1_nomask:
	v_cmp_eq_u32_e32 vcc, 0, v0
	s_and_b64 exec, exec, vcc
	s_cbranch_execz .Lp1_end
	v_mov_b32_e32 v2, 1
	s_and_b32 s3, s2, 63
	s_cmp_lt_u32 s3, 9
	s_cselect_b32 s24, 8, 7
	s_lshl_b32 s3, s3, 6
	s_add_u32 s3, s3, 8
	v_mov_b32_e32 v3, s3
	global_atomic_add v4, v3, v2, s[8:9] sc0
	s_waitcnt vmcnt(0)
	v_readfirstlane_b32 s3, v4
	s_cmp_lg_u32 s3, s24
	s_cbranch_scc1 .Lp1_end
	v_mov_b32_e32 v3, 4
	global_atomic_add v3, v2, s[8:9] offset:0
	global_atomic_add v3, v2, s[8:9] offset:64
	global_atomic_add v3, v2, s[8:9] offset:128
	global_atomic_add v3, v2, s[8:9] offset:192
	global_atomic_add v3, v2, s[8:9] offset:256
	global_atomic_add v3, v2, s[8:9] offset:320
	global_atomic_add v3, v2, s[8:9] offset:384
	global_atomic_add v3, v2, s[8:9] offset:448

.Lp2_entry:
	s_load_dwordx2 s[4:5], s[0:1], 0x10
	s_load_dwordx2 s[6:7], s[0:1], 0x18
	s_load_dwordx2 s[10:11], s[0:1], 0x28
	s_load_dwordx4 s[16:19], s[0:1], 0x30
	s_load_dwordx2 s[20:21], s[0:1], 0x40
	s_load_dwordx2 s[12:13], s[0:1], 0x50
	s_load_dwordx2 s[8:9], s[0:1], 0x20
	s_sub_i32 s33, s2, 521
	s_mov_b32 s30, 0xc350
	v_lshlrev_b32_e32 v1, 3, v0
	v_mov_b32_e32 v2, 0
	v_mov_b32_e32 v3, 0
	ds_write_b64 v1, v[2:3]
	ds_write_b64 v1, v[2:3] offset:1024
	ds_write_b64 v1, v[2:3] offset:2048
	v_mov_b32_e32 v12, 1
	v_mov_b32_e32 v19, 0
	v_mov_b32_e32 v18, 0x400
	s_waitcnt lgkmcnt(0)
	s_lshl_b32 s35, s33, 2
	s_add_u32 s24, s12, 0x41a000
	s_addc_u32 s25, s13, 0
	s_add_u32 s24, s24, s35
	s_addc_u32 s25, s25, 0
	s_add_u32 s26, s12, 0x1a000
	s_addc_u32 s27, s13, 0
	v_readfirstlane_b32 s3, v0
	s_cmp_lt_u32 s3, 64
	s_cbranch_scc0 .Lp2_polled
	s_mov_b32 s34, 0
	s_mov_b64 s[22:23], exec
	s_mov_b64 exec, 1
	s_and_b32 s3, s33, 7
	s_lshl_b32 s3, s3, 6
	s_add_u32 s3, s3, 4
	v_mov_b32_e32 v17, s3
.Lp2_poll:
	global_atomic_add v13, v17, v19, s[8:9] sc0
	s_waitcnt vmcnt(0)
	v_readfirstlane_b32 s3, v13
	s_cmpk_ge_u32 s3, 64
	s_cbranch_scc1 .Lp2_acq
	s_sleep 16
	s_add_i32 s34, s34, 1
	s_cmp_lt_u32 s34, 0x2000
	s_cbranch_scc1 .Lp2_poll
.Lp2_acq:
	s_mov_b64 exec, s[22:23]
	buffer_inv sc1
	s_waitcnt vmcnt(0)
.Lp2_polled:
	s_barrier
	v_lshlrev_b32_e32 v13, 10, v0
	global_load_dword v2, v13, s[24:25] sc1
	v_add_u32_e32 v14, 0x20000, v13
	global_load_dword v3, v14, s[24:25] sc1
	v_add_u32_e32 v14, 0x40000, v13
	global_load_dword v4, v14, s[24:25] sc1
	v_add_u32_e32 v14, 0x60000, v13
	global_load_dword v5, v14, s[24:25] sc1
	v_add_u32_e32 v14, 0x80000, v13
	v_mov_b32_e32 v6, 0
	v_cmp_gt_u32_e32 vcc, 9, v0
	s_and_saveexec_b64 s[22:23], vcc
	global_load_dword v6, v14, s[24:25] sc1
	s_mov_b64 exec, s[22:23]
	v_mul_u32_u24_e32 v13, 0x1800, v0
	s_waitcnt vmcnt(0)
	v_lshrrev_b32_e32 v7, 16, v2
	v_and_b32_e32 v2, 0xffff, v2
	v_lshl_add_u32 v2, v2, 2, v13
	v_lshrrev_b32_e32 v8, 16, v3
	v_and_b32_e32 v3, 0xffff, v3
	v_add_u32_e32 v14, 0xc0000, v13
	v_lshl_add_u32 v3, v3, 2, v14
	v_lshrrev_b32_e32 v9, 16, v4
	v_and_b32_e32 v4, 0xffff, v4
	v_add_u32_e32 v14, 0x180000, v13
	v_lshl_add_u32 v4, v4, 2, v14
	v_lshrrev_b32_e32 v10, 16, v5
	v_and_b32_e32 v5, 0xffff, v5
	v_add_u32_e32 v14, 0x240000, v13
	v_lshl_add_u32 v5, v5, 2, v14
	v_lshrrev_b32_e32 v11, 16, v6
	v_and_b32_e32 v6, 0xffff, v6
	v_add_u32_e32 v14, 0x300000, v13
	v_lshl_add_u32 v6, v6, 2, v14
	v_cmp_lt_u32_e32 vcc, 0, v7
	s_and_saveexec_b64 s[22:23], vcc
	global_load_dwordx4 v[20:23], v2, s[26:27] sc1
	v_cmp_lt_u32_e32 vcc, 4, v7
	s_and_b64 exec, exec, vcc
	global_load_dwordx4 v[24:27], v2, s[26:27] offset:16 sc1
	v_cmp_lt_u32_e32 vcc, 8, v7
	s_and_b64 exec, exec, vcc
	global_load_dwordx4 v[28:31], v2, s[26:27] offset:32 sc1
	s_mov_b64 exec, s[22:23]
	v_cmp_lt_u32_e32 vcc, 0, v8
	s_and_saveexec_b64 s[22:23], vcc
	global_load_dwordx4 v[32:35], v3, s[26:27] sc1
	v_cmp_lt_u32_e32 vcc, 4, v8
	s_and_b64 exec, exec, vcc
	global_load_dwordx4 v[36:39], v3, s[26:27] offset:16 sc1
	v_cmp_lt_u32_e32 vcc, 8, v8
	s_and_b64 exec, exec, vcc
	global_load_dwordx4 v[40:43], v3, s[26:27] offset:32 sc1
	s_mov_b64 exec, s[22:23]
	v_cmp_lt_u32_e32 vcc, 0, v9
	s_and_saveexec_b64 s[22:23], vcc
	global_load_dwordx4 v[44:47], v4, s[26:27] sc1
	v_cmp_lt_u32_e32 vcc, 4, v9
	s_and_b64 exec, exec, vcc
	global_load_dwordx4 v[48:51], v4, s[26:27] offset:16 sc1
	v_cmp_lt_u32_e32 vcc, 8, v9
	s_and_b64 exec, exec, vcc
	global_load_dwordx4 v[52:55], v4, s[26:27] offset:32 sc1
	s_mov_b64 exec, s[22:23]
	v_cmp_lt_u32_e32 vcc, 0, v10
	s_and_saveexec_b64 s[22:23], vcc
	global_load_dwordx4 v[56:59], v5, s[26:27] sc1
	v_cmp_lt_u32_e32 vcc, 4, v10
	s_and_b64 exec, exec, vcc
	global_load_dwordx4 v[60:63], v5, s[26:27] offset:16 sc1
	v_cmp_lt_u32_e32 vcc, 8, v10
	s_and_b64 exec, exec, vcc
	global_load_dwordx4 v[64:67], v5, s[26:27] offset:32 sc1
	s_mov_b64 exec, s[22:23]
	v_cmp_lt_u32_e32 vcc, 0, v11
	s_and_saveexec_b64 s[22:23], vcc
	global_load_dwordx4 v[68:71], v6, s[26:27] sc1
	v_cmp_lt_u32_e32 vcc, 4, v11
	s_and_b64 exec, exec, vcc
	global_load_dwordx4 v[72:75], v6, s[26:27] offset:16 sc1
	v_cmp_lt_u32_e32 vcc, 8, v11
	s_and_b64 exec, exec, vcc
	global_load_dwordx4 v[76:79], v6, s[26:27] offset:32 sc1
	s_mov_b64 exec, s[22:23]
	s_waitcnt vmcnt(0)
	v_cmp_lt_u32_e64 s[28:29], 4, v7
	s_cmp_lg_u64 s[28:29], 0
	s_cselect_b32 s40, 1, 0
	v_cmp_lt_u32_e64 s[28:29], 8, v7
	s_cmp_lg_u64 s[28:29], 0
	s_cselect_b32 s41, 1, 0
	v_cmp_lt_u32_e32 vcc, 0, v7
	s_and_saveexec_b64 s[22:23], vcc
	v_bfe_u32 v13, v20, 16, 8
	v_lshlrev_b32_e32 v13, 2, v13
	ds_add_rtn_u32 v80, v13, v12
	s_mov_b64 exec, s[22:23]
	v_cmp_lt_u32_e32 vcc, 1, v7
	s_and_saveexec_b64 s[22:23], vcc
	v_bfe_u32 v13, v21, 16, 8
	v_lshlrev_b32_e32 v13, 2, v13
	ds_add_rtn_u32 v81, v13, v12
	s_mov_b64 exec, s[22:23]
	v_cmp_lt_u32_e32 vcc, 2, v7
	s_and_saveexec_b64 s[22:23], vcc
	v_bfe_u32 v13, v22, 16, 8
	v_lshlrev_b32_e32 v13, 2, v13
	ds_add_rtn_u32 v82, v13, v12
	s_mov_b64 exec, s[22:23]
	v_cmp_lt_u32_e32 vcc, 3, v7
	s_and_saveexec_b64 s[22:23], vcc
	v_bfe_u32 v13, v23, 16, 8
	v_lshlrev_b32_e32 v13, 2, v13
	ds_add_rtn_u32 v83, v13, v12
	s_mov_b64 exec, s[22:23]
	s_cmp_eq_u32 s40, 0
	s_cbranch_scc1 .Lp2_c0_p1done
	v_cmp_lt_u32_e32 vcc, 4, v7
	s_and_saveexec_b64 s[22:23], vcc
	v_bfe_u32 v13, v24, 16, 8
	v_lshlrev_b32_e32 v13, 2, v13
	ds_add_rtn_u32 v84, v13, v12
	s_mov_b64 exec, s[22:23]
	v_cmp_lt_u32_e32 vcc, 5, v7
	s_and_saveexec_b64 s[22:23], vcc
	v_bfe_u32 v13, v25, 16, 8
	v_lshlrev_b32_e32 v13, 2, v13
	ds_add_rtn_u32 v85, v13, v12
	s_mov_b64 exec, s[22:23]
	v_cmp_lt_u32_e32 vcc, 6, v7
	s_and_saveexec_b64 s[22:23], vcc
	v_bfe_u32 v13, v26, 16, 8
	v_lshlrev_b32_e32 v13, 2, v13
	ds_add_rtn_u32 v86, v13, v12
	s_mov_b64 exec, s[22:23]
	v_cmp_lt_u32_e32 vcc, 7, v7
	s_and_saveexec_b64 s[22:23], vcc
	v_bfe_u32 v13, v27, 16, 8
	v_lshlrev_b32_e32 v13, 2, v13
	ds_add_rtn_u32 v87, v13, v12
	s_mov_b64 exec, s[22:23]
	s_cmp_eq_u32 s41, 0
	s_cbranch_scc1 .Lp2_c0_p1done
	v_cmp_lt_u32_e32 vcc, 8, v7
	s_and_saveexec_b64 s[22:23], vcc
	v_bfe_u32 v13, v28, 16, 8
	v_lshlrev_b32_e32 v13, 2, v13
	ds_add_rtn_u32 v88, v13, v12
	s_mov_b64 exec, s[22:23]
	v_cmp_lt_u32_e32 vcc, 9, v7
	s_and_saveexec_b64 s[22:23], vcc
	v_bfe_u32 v13, v29, 16, 8
	v_lshlrev_b32_e32 v13, 2, v13
	ds_add_rtn_u32 v89, v13, v12
	s_mov_b64 exec, s[22:23]
	v_cmp_lt_u32_e32 vcc, 10, v7
	s_and_saveexec_b64 s[22:23], vcc
	v_bfe_u32 v13, v30, 16, 8
	v_lshlrev_b32_e32 v13, 2, v13
	ds_add_rtn_u32 v90, v13, v12
	s_mov_b64 exec, s[22:23]
	v_cmp_lt_u32_e32 vcc, 11, v7
	s_and_saveexec_b64 s[22:23], vcc
	v_bfe_u32 v13, v31, 16, 8
	v_lshlrev_b32_e32 v13, 2, v13
	ds_add_rtn_u32 v91, v13, v12
	s_mov_b64 exec, s[22:23]
.Lp2_c0_p1done:
	s_waitcnt lgkmcnt(0)
	v_cmp_lt_u32_e32 vcc, 0, v7
	v_cmp_gt_u32_e64 s[28:29], 32, v80
	s_and_b64 s[28:29], s[28:29], vcc
	s_and_saveexec_b64 s[22:23], s[28:29]
	v_lshrrev_b32_e32 v13, 16, v20
	v_lshl_add_u32 v13, v13, 5, v80
	v_lshlrev_b32_e32 v13, 2, v13
	v_and_b32_e32 v14, 0xffff, v20
	global_store_dword v13, v14, s[6:7] nt
	s_mov_b64 exec, s[22:23]
	v_cmp_lt_u32_e32 vcc, 1, v7
	v_cmp_gt_u32_e64 s[28:29], 32, v81
	s_and_b64 s[28:29], s[28:29], vcc
	s_and_saveexec_b64 s[22:23], s[28:29]
	v_lshrrev_b32_e32 v13, 16, v21
	v_lshl_add_u32 v13, v13, 5, v81
	v_lshlrev_b32_e32 v13, 2, v13
	v_and_b32_e32 v14, 0xffff, v21
	global_store_dword v13, v14, s[6:7] nt
	s_mov_b64 exec, s[22:23]
	v_cmp_lt_u32_e32 vcc, 2, v7
	v_cmp_gt_u32_e64 s[28:29], 32, v82
	s_and_b64 s[28:29], s[28:29], vcc
	s_and_saveexec_b64 s[22:23], s[28:29]
	v_lshrrev_b32_e32 v13, 16, v22
	v_lshl_add_u32 v13, v13, 5, v82
	v_lshlrev_b32_e32 v13, 2, v13
	v_and_b32_e32 v14, 0xffff, v22
	global_store_dword v13, v14, s[6:7] nt
	s_mov_b64 exec, s[22:23]
	v_cmp_lt_u32_e32 vcc, 3, v7
	v_cmp_gt_u32_e64 s[28:29], 32, v83
	s_and_b64 s[28:29], s[28:29], vcc
	s_and_saveexec_b64 s[22:23], s[28:29]
	v_lshrrev_b32_e32 v13, 16, v23
	v_lshl_add_u32 v13, v13, 5, v83
	v_lshlrev_b32_e32 v13, 2, v13
	v_and_b32_e32 v14, 0xffff, v23
	global_store_dword v13, v14, s[6:7] nt
	s_mov_b64 exec, s[22:23]
	s_cmp_eq_u32 s40, 0
	s_cbranch_scc1 .Lp2_c0_p2done
	v_cmp_lt_u32_e32 vcc, 4, v7
	v_cmp_gt_u32_e64 s[28:29], 32, v84
	s_and_b64 s[28:29], s[28:29], vcc
	s_and_saveexec_b64 s[22:23], s[28:29]
	v_lshrrev_b32_e32 v13, 16, v24
	v_lshl_add_u32 v13, v13, 5, v84
	v_lshlrev_b32_e32 v13, 2, v13
	v_and_b32_e32 v14, 0xffff, v24
	global_store_dword v13, v14, s[6:7] nt
	s_mov_b64 exec, s[22:23]
	v_cmp_lt_u32_e32 vcc, 5, v7
	v_cmp_gt_u32_e64 s[28:29], 32, v85
	s_and_b64 s[28:29], s[28:29], vcc
	s_and_saveexec_b64 s[22:23], s[28:29]
	v_lshrrev_b32_e32 v13, 16, v25
	v_lshl_add_u32 v13, v13, 5, v85
	v_lshlrev_b32_e32 v13, 2, v13
	v_and_b32_e32 v14, 0xffff, v25
	global_store_dword v13, v14, s[6:7] nt
	s_mov_b64 exec, s[22:23]
	v_cmp_lt_u32_e32 vcc, 6, v7
	v_cmp_gt_u32_e64 s[28:29], 32, v86
	s_and_b64 s[28:29], s[28:29], vcc
	s_and_saveexec_b64 s[22:23], s[28:29]
	v_lshrrev_b32_e32 v13, 16, v26
	v_lshl_add_u32 v13, v13, 5, v86
	v_lshlrev_b32_e32 v13, 2, v13
	v_and_b32_e32 v14, 0xffff, v26
	global_store_dword v13, v14, s[6:7] nt
	s_mov_b64 exec, s[22:23]
	v_cmp_lt_u32_e32 vcc, 7, v7
	v_cmp_gt_u32_e64 s[28:29], 32, v87
	s_and_b64 s[28:29], s[28:29], vcc
	s_and_saveexec_b64 s[22:23], s[28:29]
	v_lshrrev_b32_e32 v13, 16, v27
	v_lshl_add_u32 v13, v13, 5, v87
	v_lshlrev_b32_e32 v13, 2, v13
	v_and_b32_e32 v14, 0xffff, v27
	global_store_dword v13, v14, s[6:7] nt
	s_mov_b64 exec, s[22:23]
	s_cmp_eq_u32 s41, 0
	s_cbranch_scc1 .Lp2_c0_p2done
	v_cmp_lt_u32_e32 vcc, 8, v7
	v_cmp_gt_u32_e64 s[28:29], 32, v88
	s_and_b64 s[28:29], s[28:29], vcc
	s_and_saveexec_b64 s[22:23], s[28:29]
	v_lshrrev_b32_e32 v13, 16, v28
	v_lshl_add_u32 v13, v13, 5, v88
	v_lshlrev_b32_e32 v13, 2, v13
	v_and_b32_e32 v14, 0xffff, v28
	global_store_dword v13, v14, s[6:7] nt
	s_mov_b64 exec, s[22:23]
	v_cmp_lt_u32_e32 vcc, 9, v7
	v_cmp_gt_u32_e64 s[28:29], 32, v89
	s_and_b64 s[28:29], s[28:29], vcc
	s_and_saveexec_b64 s[22:23], s[28:29]
	v_lshrrev_b32_e32 v13, 16, v29
	v_lshl_add_u32 v13, v13, 5, v89
	v_lshlrev_b32_e32 v13, 2, v13
	v_and_b32_e32 v14, 0xffff, v29
	global_store_dword v13, v14, s[6:7] nt
	s_mov_b64 exec, s[22:23]
	v_cmp_lt_u32_e32 vcc, 10, v7
	v_cmp_gt_u32_e64 s[28:29], 32, v90
	s_and_b64 s[28:29], s[28:29], vcc
	s_and_saveexec_b64 s[22:23], s[28:29]
	v_lshrrev_b32_e32 v13, 16, v30
	v_lshl_add_u32 v13, v13, 5, v90
	v_lshlrev_b32_e32 v13, 2, v13
	v_and_b32_e32 v14, 0xffff, v30
	global_store_dword v13, v14, s[6:7] nt
	s_mov_b64 exec, s[22:23]
	v_cmp_lt_u32_e32 vcc, 11, v7
	v_cmp_gt_u32_e64 s[28:29], 32, v91
	s_and_b64 s[28:29], s[28:29], vcc
	s_and_saveexec_b64 s[22:23], s[28:29]
	v_lshrrev_b32_e32 v13, 16, v31
	v_lshl_add_u32 v13, v13, 5, v91
	v_lshlrev_b32_e32 v13, 2, v13
	v_and_b32_e32 v14, 0xffff, v31
	global_store_dword v13, v14, s[6:7] nt
	s_mov_b64 exec, s[22:23]
.Lp2_c0_p2done:
	v_cmp_lt_u32_e64 s[28:29], 12, v7
	s_cmp_eq_u64 s[28:29], 0
	s_cbranch_scc1 .Lp2_c0_taildone
	v_mov_b32_e32 v15, 12
.Lp2_c0_tail:
	v_cmp_lt_u32_e32 vcc, v15, v7
	s_and_saveexec_b64 s[22:23], vcc
	s_cbranch_execz .Lp2_c0_tailend
	v_lshl_add_u32 v13, v15, 2, v2
	global_load_dword v16, v13, s[26:27] sc1
	s_waitcnt vmcnt(0)
	v_bfe_u32 v13, v16, 16, 8
	v_lshlrev_b32_e32 v13, 2, v13
	ds_add_rtn_u32 v17, v13, v12
	s_waitcnt lgkmcnt(0)
	v_cmp_gt_u32_e32 vcc, 32, v17
	s_and_b64 exec, exec, vcc
	v_lshrrev_b32_e32 v13, 16, v16
	v_lshl_add_u32 v13, v13, 5, v17
	v_lshlrev_b32_e32 v13, 2, v13
	v_and_b32_e32 v14, 0xffff, v16
	global_store_dword v13, v14, s[6:7] nt
	s_mov_b64 exec, s[22:23]
	v_add_u32_e32 v15, 1, v15
	s_branch .Lp2_c0_tail
.Lp2_c0_tailend:
	s_mov_b64 exec, s[22:23]
.Lp2_c0_taildone:
	v_cmp_lt_u32_e64 s[28:29], 4, v8
	s_cmp_lg_u64 s[28:29], 0
	s_cselect_b32 s40, 1, 0
	v_cmp_lt_u32_e64 s[28:29], 8, v8
	s_cmp_lg_u64 s[28:29], 0
	s_cselect_b32 s41, 1, 0
	v_cmp_lt_u32_e32 vcc, 0, v8
	s_and_saveexec_b64 s[22:23], vcc
	v_bfe_u32 v13, v32, 16, 8
	v_lshlrev_b32_e32 v13, 2, v13
	ds_add_rtn_u32 v80, v13, v12
	s_mov_b64 exec, s[22:23]
	v_cmp_lt_u32_e32 vcc, 1, v8
	s_and_saveexec_b64 s[22:23], vcc
	v_bfe_u32 v13, v33, 16, 8
	v_lshlrev_b32_e32 v13, 2, v13
	ds_add_rtn_u32 v81, v13, v12
	s_mov_b64 exec, s[22:23]
	v_cmp_lt_u32_e32 vcc, 2, v8
	s_and_saveexec_b64 s[22:23], vcc
	v_bfe_u32 v13, v34, 16, 8
	v_lshlrev_b32_e32 v13, 2, v13
	ds_add_rtn_u32 v82, v13, v12
	s_mov_b64 exec, s[22:23]
	v_cmp_lt_u32_e32 vcc, 3, v8
	s_and_saveexec_b64 s[22:23], vcc
	v_bfe_u32 v13, v35, 16, 8
	v_lshlrev_b32_e32 v13, 2, v13
	ds_add_rtn_u32 v83, v13, v12
	s_mov_b64 exec, s[22:23]
	s_cmp_eq_u32 s40, 0
	s_cbranch_scc1 .Lp2_c1_p1done
	v_cmp_lt_u32_e32 vcc, 4, v8
	s_and_saveexec_b64 s[22:23], vcc
	v_bfe_u32 v13, v36, 16, 8
	v_lshlrev_b32_e32 v13, 2, v13
	ds_add_rtn_u32 v84, v13, v12
	s_mov_b64 exec, s[22:23]
	v_cmp_lt_u32_e32 vcc, 5, v8
	s_and_saveexec_b64 s[22:23], vcc
	v_bfe_u32 v13, v37, 16, 8
	v_lshlrev_b32_e32 v13, 2, v13
	ds_add_rtn_u32 v85, v13, v12
	s_mov_b64 exec, s[22:23]
	v_cmp_lt_u32_e32 vcc, 6, v8
	s_and_saveexec_b64 s[22:23], vcc
	v_bfe_u32 v13, v38, 16, 8
	v_lshlrev_b32_e32 v13, 2, v13
	ds_add_rtn_u32 v86, v13, v12
	s_mov_b64 exec, s[22:23]
	v_cmp_lt_u32_e32 vcc, 7, v8
	s_and_saveexec_b64 s[22:23], vcc
	v_bfe_u32 v13, v39, 16, 8
	v_lshlrev_b32_e32 v13, 2, v13
	ds_add_rtn_u32 v87, v13, v12
	s_mov_b64 exec, s[22:23]
	s_cmp_eq_u32 s41, 0
	s_cbranch_scc1 .Lp2_c1_p1done
	v_cmp_lt_u32_e32 vcc, 8, v8
	s_and_saveexec_b64 s[22:23], vcc
	v_bfe_u32 v13, v40, 16, 8
	v_lshlrev_b32_e32 v13, 2, v13
	ds_add_rtn_u32 v88, v13, v12
	s_mov_b64 exec, s[22:23]
	v_cmp_lt_u32_e32 vcc, 9, v8
	s_and_saveexec_b64 s[22:23], vcc
	v_bfe_u32 v13, v41, 16, 8
	v_lshlrev_b32_e32 v13, 2, v13
	ds_add_rtn_u32 v89, v13, v12
	s_mov_b64 exec, s[22:23]
	v_cmp_lt_u32_e32 vcc, 10, v8
	s_and_saveexec_b64 s[22:23], vcc
	v_bfe_u32 v13, v42, 16, 8
	v_lshlrev_b32_e32 v13, 2, v13
	ds_add_rtn_u32 v90, v13, v12
	s_mov_b64 exec, s[22:23]
	v_cmp_lt_u32_e32 vcc, 11, v8
	s_and_saveexec_b64 s[22:23], vcc
	v_bfe_u32 v13, v43, 16, 8
	v_lshlrev_b32_e32 v13, 2, v13
	ds_add_rtn_u32 v91, v13, v12
	s_mov_b64 exec, s[22:23]
.Lp2_c1_p1done:
	s_waitcnt lgkmcnt(0)
	v_cmp_lt_u32_e32 vcc, 0, v8
	v_cmp_gt_u32_e64 s[28:29], 32, v80
	s_and_b64 s[28:29], s[28:29], vcc
	s_and_saveexec_b64 s[22:23], s[28:29]
	v_lshrrev_b32_e32 v13, 16, v32
	v_lshl_add_u32 v13, v13, 5, v80
	v_lshlrev_b32_e32 v13, 2, v13
	v_and_b32_e32 v14, 0xffff, v32
	global_store_dword v13, v14, s[6:7] nt
	s_mov_b64 exec, s[22:23]
	v_cmp_lt_u32_e32 vcc, 1, v8
	v_cmp_gt_u32_e64 s[28:29], 32, v81
	s_and_b64 s[28:29], s[28:29], vcc
	s_and_saveexec_b64 s[22:23], s[28:29]
	v_lshrrev_b32_e32 v13, 16, v33
	v_lshl_add_u32 v13, v13, 5, v81
	v_lshlrev_b32_e32 v13, 2, v13
	v_and_b32_e32 v14, 0xffff, v33
	global_store_dword v13, v14, s[6:7] nt
	s_mov_b64 exec, s[22:23]
	v_cmp_lt_u32_e32 vcc, 2, v8
	v_cmp_gt_u32_e64 s[28:29], 32, v82
	s_and_b64 s[28:29], s[28:29], vcc
	s_and_saveexec_b64 s[22:23], s[28:29]
	v_lshrrev_b32_e32 v13, 16, v34
	v_lshl_add_u32 v13, v13, 5, v82
	v_lshlrev_b32_e32 v13, 2, v13
	v_and_b32_e32 v14, 0xffff, v34
	global_store_dword v13, v14, s[6:7] nt
	s_mov_b64 exec, s[22:23]
	v_cmp_lt_u32_e32 vcc, 3, v8
	v_cmp_gt_u32_e64 s[28:29], 32, v83
	s_and_b64 s[28:29], s[28:29], vcc
	s_and_saveexec_b64 s[22:23], s[28:29]
	v_lshrrev_b32_e32 v13, 16, v35
	v_lshl_add_u32 v13, v13, 5, v83
	v_lshlrev_b32_e32 v13, 2, v13
	v_and_b32_e32 v14, 0xffff, v35
	global_store_dword v13, v14, s[6:7] nt
	s_mov_b64 exec, s[22:23]
	s_cmp_eq_u32 s40, 0
	s_cbranch_scc1 .Lp2_c1_p2done
	v_cmp_lt_u32_e32 vcc, 4, v8
	v_cmp_gt_u32_e64 s[28:29], 32, v84
	s_and_b64 s[28:29], s[28:29], vcc
	s_and_saveexec_b64 s[22:23], s[28:29]
	v_lshrrev_b32_e32 v13, 16, v36
	v_lshl_add_u32 v13, v13, 5, v84
	v_lshlrev_b32_e32 v13, 2, v13
	v_and_b32_e32 v14, 0xffff, v36
	global_store_dword v13, v14, s[6:7] nt
	s_mov_b64 exec, s[22:23]
	v_cmp_lt_u32_e32 vcc, 5, v8
	v_cmp_gt_u32_e64 s[28:29], 32, v85
	s_and_b64 s[28:29], s[28:29], vcc
	s_and_saveexec_b64 s[22:23], s[28:29]
	v_lshrrev_b32_e32 v13, 16, v37
	v_lshl_add_u32 v13, v13, 5, v85
	v_lshlrev_b32_e32 v13, 2, v13
	v_and_b32_e32 v14, 0xffff, v37
	global_store_dword v13, v14, s[6:7] nt
	s_mov_b64 exec, s[22:23]
	v_cmp_lt_u32_e32 vcc, 6, v8
	v_cmp_gt_u32_e64 s[28:29], 32, v86
	s_and_b64 s[28:29], s[28:29], vcc
	s_and_saveexec_b64 s[22:23], s[28:29]
	v_lshrrev_b32_e32 v13, 16, v38
	v_lshl_add_u32 v13, v13, 5, v86
	v_lshlrev_b32_e32 v13, 2, v13
	v_and_b32_e32 v14, 0xffff, v38
	global_store_dword v13, v14, s[6:7] nt
	s_mov_b64 exec, s[22:23]
	v_cmp_lt_u32_e32 vcc, 7, v8
	v_cmp_gt_u32_e64 s[28:29], 32, v87
	s_and_b64 s[28:29], s[28:29], vcc
	s_and_saveexec_b64 s[22:23], s[28:29]
	v_lshrrev_b32_e32 v13, 16, v39
	v_lshl_add_u32 v13, v13, 5, v87
	v_lshlrev_b32_e32 v13, 2, v13
	v_and_b32_e32 v14, 0xffff, v39
	global_store_dword v13, v14, s[6:7] nt
	s_mov_b64 exec, s[22:23]
	s_cmp_eq_u32 s41, 0
	s_cbranch_scc1 .Lp2_c1_p2done
	v_cmp_lt_u32_e32 vcc, 8, v8
	v_cmp_gt_u32_e64 s[28:29], 32, v88
	s_and_b64 s[28:29], s[28:29], vcc
	s_and_saveexec_b64 s[22:23], s[28:29]
	v_lshrrev_b32_e32 v13, 16, v40
	v_lshl_add_u32 v13, v13, 5, v88
	v_lshlrev_b32_e32 v13, 2, v13
	v_and_b32_e32 v14, 0xffff, v40
	global_store_dword v13, v14, s[6:7] nt
	s_mov_b64 exec, s[22:23]
	v_cmp_lt_u32_e32 vcc, 9, v8
	v_cmp_gt_u32_e64 s[28:29], 32, v89
	s_and_b64 s[28:29], s[28:29], vcc
	s_and_saveexec_b64 s[22:23], s[28:29]
	v_lshrrev_b32_e32 v13, 16, v41
	v_lshl_add_u32 v13, v13, 5, v89
	v_lshlrev_b32_e32 v13, 2, v13
	v_and_b32_e32 v14, 0xffff, v41
	global_store_dword v13, v14, s[6:7] nt
	s_mov_b64 exec, s[22:23]
	v_cmp_lt_u32_e32 vcc, 10, v8
	v_cmp_gt_u32_e64 s[28:29], 32, v90
	s_and_b64 s[28:29], s[28:29], vcc
	s_and_saveexec_b64 s[22:23], s[28:29]
	v_lshrrev_b32_e32 v13, 16, v42
	v_lshl_add_u32 v13, v13, 5, v90
	v_lshlrev_b32_e32 v13, 2, v13
	v_and_b32_e32 v14, 0xffff, v42
	global_store_dword v13, v14, s[6:7] nt
	s_mov_b64 exec, s[22:23]
	v_cmp_lt_u32_e32 vcc, 11, v8
	v_cmp_gt_u32_e64 s[28:29], 32, v91
	s_and_b64 s[28:29], s[28:29], vcc
	s_and_saveexec_b64 s[22:23], s[28:29]
	v_lshrrev_b32_e32 v13, 16, v43
	v_lshl_add_u32 v13, v13, 5, v91
	v_lshlrev_b32_e32 v13, 2, v13
	v_and_b32_e32 v14, 0xffff, v43
	global_store_dword v13, v14, s[6:7] nt
	s_mov_b64 exec, s[22:23]
.Lp2_c1_p2done:
	v_cmp_lt_u32_e64 s[28:29], 12, v8
	s_cmp_eq_u64 s[28:29], 0
	s_cbranch_scc1 .Lp2_c1_taildone
	v_mov_b32_e32 v15, 12
.Lp2_c1_tail:
	v_cmp_lt_u32_e32 vcc, v15, v8
	s_and_saveexec_b64 s[22:23], vcc
	s_cbranch_execz .Lp2_c1_tailend
	v_lshl_add_u32 v13, v15, 2, v3
	global_load_dword v16, v13, s[26:27] sc1
	s_waitcnt vmcnt(0)
	v_bfe_u32 v13, v16, 16, 8
	v_lshlrev_b32_e32 v13, 2, v13
	ds_add_rtn_u32 v17, v13, v12
	s_waitcnt lgkmcnt(0)
	v_cmp_gt_u32_e32 vcc, 32, v17
	s_and_b64 exec, exec, vcc
	v_lshrrev_b32_e32 v13, 16, v16
	v_lshl_add_u32 v13, v13, 5, v17
	v_lshlrev_b32_e32 v13, 2, v13
	v_and_b32_e32 v14, 0xffff, v16
	global_store_dword v13, v14, s[6:7] nt
	s_mov_b64 exec, s[22:23]
	v_add_u32_e32 v15, 1, v15
	s_branch .Lp2_c1_tail

.Lp2_c1_taildone:
	v_cmp_lt_u32_e64 s[28:29], 4, v9
	s_cmp_lg_u64 s[28:29], 0
	s_cselect_b32 s40, 1, 0
	v_cmp_lt_u32_e64 s[28:29], 8, v9
	s_cmp_lg_u64 s[28:29], 0
	s_cselect_b32 s41, 1, 0
	v_cmp_lt_u32_e32 vcc, 0, v9
	s_and_saveexec_b64 s[22:23], vcc
	v_bfe_u32 v13, v44, 16, 8
	v_lshlrev_b32_e32 v13, 2, v13
	ds_add_rtn_u32 v80, v13, v12
	s_mov_b64 exec, s[22:23]
	v_cmp_lt_u32_e32 vcc, 1, v9
	s_and_saveexec_b64 s[22:23], vcc
	v_bfe_u32 v13, v45, 16, 8
	v_lshlrev_b32_e32 v13, 2, v13
	ds_add_rtn_u32 v81, v13, v12
	s_mov_b64 exec, s[22:23]
	v_cmp_lt_u32_e32 vcc, 2, v9
	s_and_saveexec_b64 s[22:23], vcc
	v_bfe_u32 v13, v46, 16, 8
	v_lshlrev_b32_e32 v13, 2, v13
	ds_add_rtn_u32 v82, v13, v12
	s_mov_b64 exec, s[22:23]
	v_cmp_lt_u32_e32 vcc, 3, v9
	s_and_saveexec_b64 s[22:23], vcc
	v_bfe_u32 v13, v47, 16, 8
	v_lshlrev_b32_e32 v13, 2, v13
	ds_add_rtn_u32 v83, v13, v12
	s_mov_b64 exec, s[22:23]
	s_cmp_eq_u32 s40, 0
	s_cbranch_scc1 .Lp2_c2_p1done
	v_cmp_lt_u32_e32 vcc, 4, v9
	s_and_saveexec_b64 s[22:23], vcc
	v_bfe_u32 v13, v48, 16, 8
	v_lshlrev_b32_e32 v13, 2, v13
	ds_add_rtn_u32 v84, v13, v12
	s_mov_b64 exec, s[22:23]
	v_cmp_lt_u32_e32 vcc, 5, v9
	s_and_saveexec_b64 s[22:23], vcc
	v_bfe_u32 v13, v49, 16, 8
	v_lshlrev_b32_e32 v13, 2, v13
	ds_add_rtn_u32 v85, v13, v12
	s_mov_b64 exec, s[22:23]
	v_cmp_lt_u32_e32 vcc, 6, v9
	s_and_saveexec_b64 s[22:23], vcc
	v_bfe_u32 v13, v50, 16, 8
	v_lshlrev_b32_e32 v13, 2, v13
	ds_add_rtn_u32 v86, v13, v12
	s_mov_b64 exec, s[22:23]
	v_cmp_lt_u32_e32 vcc, 7, v9
	s_and_saveexec_b64 s[22:23], vcc
	v_bfe_u32 v13, v51, 16, 8
	v_lshlrev_b32_e32 v13, 2, v13
	ds_add_rtn_u32 v87, v13, v12
	s_mov_b64 exec, s[22:23]
	s_cmp_eq_u32 s41, 0
	s_cbranch_scc1 .Lp2_c2_p1done
	v_cmp_lt_u32_e32 vcc, 8, v9
	s_and_saveexec_b64 s[22:23], vcc
	v_bfe_u32 v13, v52, 16, 8
	v_lshlrev_b32_e32 v13, 2, v13
	ds_add_rtn_u32 v88, v13, v12
	s_mov_b64 exec, s[22:23]
	v_cmp_lt_u32_e32 vcc, 9, v9
	s_and_saveexec_b64 s[22:23], vcc
	v_bfe_u32 v13, v53, 16, 8
	v_lshlrev_b32_e32 v13, 2, v13
	ds_add_rtn_u32 v89, v13, v12
	s_mov_b64 exec, s[22:23]
	v_cmp_lt_u32_e32 vcc, 10, v9
	s_and_saveexec_b64 s[22:23], vcc
	v_bfe_u32 v13, v54, 16, 8
	v_lshlrev_b32_e32 v13, 2, v13
	ds_add_rtn_u32 v90, v13, v12
	s_mov_b64 exec, s[22:23]
	v_cmp_lt_u32_e32 vcc, 11, v9
	s_and_saveexec_b64 s[22:23], vcc
	v_bfe_u32 v13, v55, 16, 8
	v_lshlrev_b32_e32 v13, 2, v13
	ds_add_rtn_u32 v91, v13, v12
	s_mov_b64 exec, s[22:23]
.Lp2_c2_p1done:
	s_waitcnt lgkmcnt(0)
	v_cmp_lt_u32_e32 vcc, 0, v9
	v_cmp_gt_u32_e64 s[28:29], 32, v80
	s_and_b64 s[28:29], s[28:29], vcc
	s_and_saveexec_b64 s[22:23], s[28:29]
	v_lshrrev_b32_e32 v13, 16, v44
	v_lshl_add_u32 v13, v13, 5, v80
	v_lshlrev_b32_e32 v13, 2, v13
	v_and_b32_e32 v14, 0xffff, v44
	global_store_dword v13, v14, s[6:7] nt
	s_mov_b64 exec, s[22:23]
	v_cmp_lt_u32_e32 vcc, 1, v9
	v_cmp_gt_u32_e64 s[28:29], 32, v81
	s_and_b64 s[28:29], s[28:29], vcc
	s_and_saveexec_b64 s[22:23], s[28:29]
	v_lshrrev_b32_e32 v13, 16, v45
	v_lshl_add_u32 v13, v13, 5, v81
	v_lshlrev_b32_e32 v13, 2, v13
	v_and_b32_e32 v14, 0xffff, v45
	global_store_dword v13, v14, s[6:7] nt
	s_mov_b64 exec, s[22:23]
	v_cmp_lt_u32_e32 vcc, 2, v9
	v_cmp_gt_u32_e64 s[28:29], 32, v82
	s_and_b64 s[28:29], s[28:29], vcc
	s_and_saveexec_b64 s[22:23], s[28:29]
	v_lshrrev_b32_e32 v13, 16, v46
	v_lshl_add_u32 v13, v13, 5, v82
	v_lshlrev_b32_e32 v13, 2, v13
	v_and_b32_e32 v14, 0xffff, v46
	global_store_dword v13, v14, s[6:7] nt
	s_mov_b64 exec, s[22:23]
	v_cmp_lt_u32_e32 vcc, 3, v9
	v_cmp_gt_u32_e64 s[28:29], 32, v83
	s_and_b64 s[28:29], s[28:29], vcc
	s_and_saveexec_b64 s[22:23], s[28:29]
	v_lshrrev_b32_e32 v13, 16, v47
	v_lshl_add_u32 v13, v13, 5, v83
	v_lshlrev_b32_e32 v13, 2, v13
	v_and_b32_e32 v14, 0xffff, v47
	global_store_dword v13, v14, s[6:7] nt
	s_mov_b64 exec, s[22:23]
	s_cmp_eq_u32 s40, 0
	s_cbranch_scc1 .Lp2_c2_p2done
	v_cmp_lt_u32_e32 vcc, 4, v9
	v_cmp_gt_u32_e64 s[28:29], 32, v84
	s_and_b64 s[28:29], s[28:29], vcc
	s_and_saveexec_b64 s[22:23], s[28:29]
	v_lshrrev_b32_e32 v13, 16, v48
	v_lshl_add_u32 v13, v13, 5, v84
	v_lshlrev_b32_e32 v13, 2, v13
	v_and_b32_e32 v14, 0xffff, v48
	global_store_dword v13, v14, s[6:7] nt
	s_mov_b64 exec, s[22:23]
	v_cmp_lt_u32_e32 vcc, 5, v9
	v_cmp_gt_u32_e64 s[28:29], 32, v85
	s_and_b64 s[28:29], s[28:29], vcc
	s_and_saveexec_b64 s[22:23], s[28:29]
	v_lshrrev_b32_e32 v13, 16, v49
	v_lshl_add_u32 v13, v13, 5, v85
	v_lshlrev_b32_e32 v13, 2, v13
	v_and_b32_e32 v14, 0xffff, v49
	global_store_dword v13, v14, s[6:7] nt
	s_mov_b64 exec, s[22:23]
	v_cmp_lt_u32_e32 vcc, 6, v9
	v_cmp_gt_u32_e64 s[28:29], 32, v86
	s_and_b64 s[28:29], s[28:29], vcc
	s_and_saveexec_b64 s[22:23], s[28:29]
	v_lshrrev_b32_e32 v13, 16, v50
	v_lshl_add_u32 v13, v13, 5, v86
	v_lshlrev_b32_e32 v13, 2, v13
	v_and_b32_e32 v14, 0xffff, v50
	global_store_dword v13, v14, s[6:7] nt
	s_mov_b64 exec, s[22:23]
	v_cmp_lt_u32_e32 vcc, 7, v9
	v_cmp_gt_u32_e64 s[28:29], 32, v87
	s_and_b64 s[28:29], s[28:29], vcc
	s_and_saveexec_b64 s[22:23], s[28:29]
	v_lshrrev_b32_e32 v13, 16, v51
	v_lshl_add_u32 v13, v13, 5, v87
	v_lshlrev_b32_e32 v13, 2, v13
	v_and_b32_e32 v14, 0xffff, v51
	global_store_dword v13, v14, s[6:7] nt
	s_mov_b64 exec, s[22:23]
	s_cmp_eq_u32 s41, 0
	s_cbranch_scc1 .Lp2_c2_p2done
	v_cmp_lt_u32_e32 vcc, 8, v9
	v_cmp_gt_u32_e64 s[28:29], 32, v88
	s_and_b64 s[28:29], s[28:29], vcc
	s_and_saveexec_b64 s[22:23], s[28:29]
	v_lshrrev_b32_e32 v13, 16, v52
	v_lshl_add_u32 v13, v13, 5, v88
	v_lshlrev_b32_e32 v13, 2, v13
	v_and_b32_e32 v14, 0xffff, v52
	global_store_dword v13, v14, s[6:7] nt
	s_mov_b64 exec, s[22:23]
	v_cmp_lt_u32_e32 vcc, 9, v9
	v_cmp_gt_u32_e64 s[28:29], 32, v89
	s_and_b64 s[28:29], s[28:29], vcc
	s_and_saveexec_b64 s[22:23], s[28:29]
	v_lshrrev_b32_e32 v13, 16, v53
	v_lshl_add_u32 v13, v13, 5, v89
	v_lshlrev_b32_e32 v13, 2, v13
	v_and_b32_e32 v14, 0xffff, v53
	global_store_dword v13, v14, s[6:7] nt
	s_mov_b64 exec, s[22:23]
	v_cmp_lt_u32_e32 vcc, 10, v9
	v_cmp_gt_u32_e64 s[28:29], 32, v90
	s_and_b64 s[28:29], s[28:29], vcc
	s_and_saveexec_b64 s[22:23], s[28:29]
	v_lshrrev_b32_e32 v13, 16, v54
	v_lshl_add_u32 v13, v13, 5, v90
	v_lshlrev_b32_e32 v13, 2, v13
	v_and_b32_e32 v14, 0xffff, v54
	global_store_dword v13, v14, s[6:7] nt
	s_mov_b64 exec, s[22:23]
	v_cmp_lt_u32_e32 vcc, 11, v9
	v_cmp_gt_u32_e64 s[28:29], 32, v91
	s_and_b64 s[28:29], s[28:29], vcc
	s_and_saveexec_b64 s[22:23], s[28:29]
	v_lshrrev_b32_e32 v13, 16, v55
	v_lshl_add_u32 v13, v13, 5, v91
	v_lshlrev_b32_e32 v13, 2, v13
	v_and_b32_e32 v14, 0xffff, v55
	global_store_dword v13, v14, s[6:7] nt
	s_mov_b64 exec, s[22:23]
.Lp2_c2_p2done:
	v_cmp_lt_u32_e64 s[28:29], 12, v9
	s_cmp_eq_u64 s[28:29], 0
	s_cbranch_scc1 .Lp2_c2_taildone
	v_mov_b32_e32 v15, 12
.Lp2_c2_tail:
	v_cmp_lt_u32_e32 vcc, v15, v9
	s_and_saveexec_b64 s[22:23], vcc
	s_cbranch_execz .Lp2_c2_tailend
	v_lshl_add_u32 v13, v15, 2, v4
	global_load_dword v16, v13, s[26:27] sc1
	s_waitcnt vmcnt(0)
	v_bfe_u32 v13, v16, 16, 8
	v_lshlrev_b32_e32 v13, 2, v13
	ds_add_rtn_u32 v17, v13, v12
	s_waitcnt lgkmcnt(0)
	v_cmp_gt_u32_e32 vcc, 32, v17
	s_and_b64 exec, exec, vcc
	v_lshrrev_b32_e32 v13, 16, v16
	v_lshl_add_u32 v13, v13, 5, v17
	v_lshlrev_b32_e32 v13, 2, v13
	v_and_b32_e32 v14, 0xffff, v16
	global_store_dword v13, v14, s[6:7] nt
	s_mov_b64 exec, s[22:23]
	v_add_u32_e32 v15, 1, v15
	s_branch .Lp2_c2_tail

.Lp2_c2_taildone:
	v_cmp_lt_u32_e64 s[28:29], 4, v10
	s_cmp_lg_u64 s[28:29], 0
	s_cselect_b32 s40, 1, 0
	v_cmp_lt_u32_e64 s[28:29], 8, v10
	s_cmp_lg_u64 s[28:29], 0
	s_cselect_b32 s41, 1, 0
	v_cmp_lt_u32_e32 vcc, 0, v10
	s_and_saveexec_b64 s[22:23], vcc
	v_bfe_u32 v13, v56, 16, 8
	v_lshlrev_b32_e32 v13, 2, v13
	ds_add_rtn_u32 v80, v13, v12
	s_mov_b64 exec, s[22:23]
	v_cmp_lt_u32_e32 vcc, 1, v10
	s_and_saveexec_b64 s[22:23], vcc
	v_bfe_u32 v13, v57, 16, 8
	v_lshlrev_b32_e32 v13, 2, v13
	ds_add_rtn_u32 v81, v13, v12
	s_mov_b64 exec, s[22:23]
	v_cmp_lt_u32_e32 vcc, 2, v10
	s_and_saveexec_b64 s[22:23], vcc
	v_bfe_u32 v13, v58, 16, 8
	v_lshlrev_b32_e32 v13, 2, v13
	ds_add_rtn_u32 v82, v13, v12
	s_mov_b64 exec, s[22:23]
	v_cmp_lt_u32_e32 vcc, 3, v10
	s_and_saveexec_b64 s[22:23], vcc
	v_bfe_u32 v13, v59, 16, 8
	v_lshlrev_b32_e32 v13, 2, v13
	ds_add_rtn_u32 v83, v13, v12
	s_mov_b64 exec, s[22:23]
	s_cmp_eq_u32 s40, 0
	s_cbranch_scc1 .Lp2_c3_p1done
	v_cmp_lt_u32_e32 vcc, 4, v10
	s_and_saveexec_b64 s[22:23], vcc
	v_bfe_u32 v13, v60, 16, 8
	v_lshlrev_b32_e32 v13, 2, v13
	ds_add_rtn_u32 v84, v13, v12
	s_mov_b64 exec, s[22:23]
	v_cmp_lt_u32_e32 vcc, 5, v10
	s_and_saveexec_b64 s[22:23], vcc
	v_bfe_u32 v13, v61, 16, 8
	v_lshlrev_b32_e32 v13, 2, v13
	ds_add_rtn_u32 v85, v13, v12
	s_mov_b64 exec, s[22:23]
	v_cmp_lt_u32_e32 vcc, 6, v10
	s_and_saveexec_b64 s[22:23], vcc
	v_bfe_u32 v13, v62, 16, 8
	v_lshlrev_b32_e32 v13, 2, v13
	ds_add_rtn_u32 v86, v13, v12
	s_mov_b64 exec, s[22:23]
	v_cmp_lt_u32_e32 vcc, 7, v10
	s_and_saveexec_b64 s[22:23], vcc
	v_bfe_u32 v13, v63, 16, 8
	v_lshlrev_b32_e32 v13, 2, v13
	ds_add_rtn_u32 v87, v13, v12
	s_mov_b64 exec, s[22:23]
	s_cmp_eq_u32 s41, 0
	s_cbranch_scc1 .Lp2_c3_p1done
	v_cmp_lt_u32_e32 vcc, 8, v10
	s_and_saveexec_b64 s[22:23], vcc
	v_bfe_u32 v13, v64, 16, 8
	v_lshlrev_b32_e32 v13, 2, v13
	ds_add_rtn_u32 v88, v13, v12
	s_mov_b64 exec, s[22:23]
	v_cmp_lt_u32_e32 vcc, 9, v10
	s_and_saveexec_b64 s[22:23], vcc
	v_bfe_u32 v13, v65, 16, 8
	v_lshlrev_b32_e32 v13, 2, v13
	ds_add_rtn_u32 v89, v13, v12
	s_mov_b64 exec, s[22:23]
	v_cmp_lt_u32_e32 vcc, 10, v10
	s_and_saveexec_b64 s[22:23], vcc
	v_bfe_u32 v13, v66, 16, 8
	v_lshlrev_b32_e32 v13, 2, v13
	ds_add_rtn_u32 v90, v13, v12
	s_mov_b64 exec, s[22:23]
	v_cmp_lt_u32_e32 vcc, 11, v10
	s_and_saveexec_b64 s[22:23], vcc
	v_bfe_u32 v13, v67, 16, 8
	v_lshlrev_b32_e32 v13, 2, v13
	ds_add_rtn_u32 v91, v13, v12
	s_mov_b64 exec, s[22:23]
.Lp2_c3_p1done:
	s_waitcnt lgkmcnt(0)
	v_cmp_lt_u32_e32 vcc, 0, v10
	v_cmp_gt_u32_e64 s[28:29], 32, v80
	s_and_b64 s[28:29], s[28:29], vcc
	s_and_saveexec_b64 s[22:23], s[28:29]
	v_lshrrev_b32_e32 v13, 16, v56
	v_lshl_add_u32 v13, v13, 5, v80
	v_lshlrev_b32_e32 v13, 2, v13
	v_and_b32_e32 v14, 0xffff, v56
	global_store_dword v13, v14, s[6:7] nt
	s_mov_b64 exec, s[22:23]
	v_cmp_lt_u32_e32 vcc, 1, v10
	v_cmp_gt_u32_e64 s[28:29], 32, v81
	s_and_b64 s[28:29], s[28:29], vcc
	s_and_saveexec_b64 s[22:23], s[28:29]
	v_lshrrev_b32_e32 v13, 16, v57
	v_lshl_add_u32 v13, v13, 5, v81
	v_lshlrev_b32_e32 v13, 2, v13
	v_and_b32_e32 v14, 0xffff, v57
	global_store_dword v13, v14, s[6:7] nt
	s_mov_b64 exec, s[22:23]
	v_cmp_lt_u32_e32 vcc, 2, v10
	v_cmp_gt_u32_e64 s[28:29], 32, v82
	s_and_b64 s[28:29], s[28:29], vcc
	s_and_saveexec_b64 s[22:23], s[28:29]
	v_lshrrev_b32_e32 v13, 16, v58
	v_lshl_add_u32 v13, v13, 5, v82
	v_lshlrev_b32_e32 v13, 2, v13
	v_and_b32_e32 v14, 0xffff, v58
	global_store_dword v13, v14, s[6:7] nt
	s_mov_b64 exec, s[22:23]
	v_cmp_lt_u32_e32 vcc, 3, v10
	v_cmp_gt_u32_e64 s[28:29], 32, v83
	s_and_b64 s[28:29], s[28:29], vcc
	s_and_saveexec_b64 s[22:23], s[28:29]
	v_lshrrev_b32_e32 v13, 16, v59
	v_lshl_add_u32 v13, v13, 5, v83
	v_lshlrev_b32_e32 v13, 2, v13
	v_and_b32_e32 v14, 0xffff, v59
	global_store_dword v13, v14, s[6:7] nt
	s_mov_b64 exec, s[22:23]
	s_cmp_eq_u32 s40, 0
	s_cbranch_scc1 .Lp2_c3_p2done
	v_cmp_lt_u32_e32 vcc, 4, v10
	v_cmp_gt_u32_e64 s[28:29], 32, v84
	s_and_b64 s[28:29], s[28:29], vcc
	s_and_saveexec_b64 s[22:23], s[28:29]
	v_lshrrev_b32_e32 v13, 16, v60
	v_lshl_add_u32 v13, v13, 5, v84
	v_lshlrev_b32_e32 v13, 2, v13
	v_and_b32_e32 v14, 0xffff, v60
	global_store_dword v13, v14, s[6:7] nt
	s_mov_b64 exec, s[22:23]
	v_cmp_lt_u32_e32 vcc, 5, v10
	v_cmp_gt_u32_e64 s[28:29], 32, v85
	s_and_b64 s[28:29], s[28:29], vcc
	s_and_saveexec_b64 s[22:23], s[28:29]
	v_lshrrev_b32_e32 v13, 16, v61
	v_lshl_add_u32 v13, v13, 5, v85
	v_lshlrev_b32_e32 v13, 2, v13
	v_and_b32_e32 v14, 0xffff, v61
	global_store_dword v13, v14, s[6:7] nt
	s_mov_b64 exec, s[22:23]
	v_cmp_lt_u32_e32 vcc, 6, v10
	v_cmp_gt_u32_e64 s[28:29], 32, v86
	s_and_b64 s[28:29], s[28:29], vcc
	s_and_saveexec_b64 s[22:23], s[28:29]
	v_lshrrev_b32_e32 v13, 16, v62
	v_lshl_add_u32 v13, v13, 5, v86
	v_lshlrev_b32_e32 v13, 2, v13
	v_and_b32_e32 v14, 0xffff, v62
	global_store_dword v13, v14, s[6:7] nt
	s_mov_b64 exec, s[22:23]
	v_cmp_lt_u32_e32 vcc, 7, v10
	v_cmp_gt_u32_e64 s[28:29], 32, v87
	s_and_b64 s[28:29], s[28:29], vcc
	s_and_saveexec_b64 s[22:23], s[28:29]
	v_lshrrev_b32_e32 v13, 16, v63
	v_lshl_add_u32 v13, v13, 5, v87
	v_lshlrev_b32_e32 v13, 2, v13
	v_and_b32_e32 v14, 0xffff, v63
	global_store_dword v13, v14, s[6:7] nt
	s_mov_b64 exec, s[22:23]
	s_cmp_eq_u32 s41, 0
	s_cbranch_scc1 .Lp2_c3_p2done
	v_cmp_lt_u32_e32 vcc, 8, v10
	v_cmp_gt_u32_e64 s[28:29], 32, v88
	s_and_b64 s[28:29], s[28:29], vcc
	s_and_saveexec_b64 s[22:23], s[28:29]
	v_lshrrev_b32_e32 v13, 16, v64
	v_lshl_add_u32 v13, v13, 5, v88
	v_lshlrev_b32_e32 v13, 2, v13
	v_and_b32_e32 v14, 0xffff, v64
	global_store_dword v13, v14, s[6:7] nt
	s_mov_b64 exec, s[22:23]
	v_cmp_lt_u32_e32 vcc, 9, v10
	v_cmp_gt_u32_e64 s[28:29], 32, v89
	s_and_b64 s[28:29], s[28:29], vcc
	s_and_saveexec_b64 s[22:23], s[28:29]
	v_lshrrev_b32_e32 v13, 16, v65
	v_lshl_add_u32 v13, v13, 5, v89
	v_lshlrev_b32_e32 v13, 2, v13
	v_and_b32_e32 v14, 0xffff, v65
	global_store_dword v13, v14, s[6:7] nt
	s_mov_b64 exec, s[22:23]
	v_cmp_lt_u32_e32 vcc, 10, v10
	v_cmp_gt_u32_e64 s[28:29], 32, v90
	s_and_b64 s[28:29], s[28:29], vcc
	s_and_saveexec_b64 s[22:23], s[28:29]
	v_lshrrev_b32_e32 v13, 16, v66
	v_lshl_add_u32 v13, v13, 5, v90
	v_lshlrev_b32_e32 v13, 2, v13
	v_and_b32_e32 v14, 0xffff, v66
	global_store_dword v13, v14, s[6:7] nt
	s_mov_b64 exec, s[22:23]
	v_cmp_lt_u32_e32 vcc, 11, v10
	v_cmp_gt_u32_e64 s[28:29], 32, v91
	s_and_b64 s[28:29], s[28:29], vcc
	s_and_saveexec_b64 s[22:23], s[28:29]
	v_lshrrev_b32_e32 v13, 16, v67
	v_lshl_add_u32 v13, v13, 5, v91
	v_lshlrev_b32_e32 v13, 2, v13
	v_and_b32_e32 v14, 0xffff, v67
	global_store_dword v13, v14, s[6:7] nt
	s_mov_b64 exec, s[22:23]
.Lp2_c3_p2done:
	v_cmp_lt_u32_e64 s[28:29], 12, v10
	s_cmp_eq_u64 s[28:29], 0
	s_cbranch_scc1 .Lp2_c3_taildone
	v_mov_b32_e32 v15, 12
.Lp2_c3_tail:
	v_cmp_lt_u32_e32 vcc, v15, v10
	s_and_saveexec_b64 s[22:23], vcc
	s_cbranch_execz .Lp2_c3_tailend
	v_lshl_add_u32 v13, v15, 2, v5
	global_load_dword v16, v13, s[26:27] sc1
	s_waitcnt vmcnt(0)
	v_bfe_u32 v13, v16, 16, 8
	v_lshlrev_b32_e32 v13, 2, v13
	ds_add_rtn_u32 v17, v13, v12
	s_waitcnt lgkmcnt(0)
	v_cmp_gt_u32_e32 vcc, 32, v17
	s_and_b64 exec, exec, vcc
	v_lshrrev_b32_e32 v13, 16, v16
	v_lshl_add_u32 v13, v13, 5, v17
	v_lshlrev_b32_e32 v13, 2, v13
	v_and_b32_e32 v14, 0xffff, v16
	global_store_dword v13, v14, s[6:7] nt
	s_mov_b64 exec, s[22:23]
	v_add_u32_e32 v15, 1, v15
	s_branch .Lp2_c3_tail

.Lp2_c3_taildone:
	v_cmp_lt_u32_e64 s[28:29], 4, v11
	s_cmp_lg_u64 s[28:29], 0
	s_cselect_b32 s40, 1, 0
	v_cmp_lt_u32_e64 s[28:29], 8, v11
	s_cmp_lg_u64 s[28:29], 0
	s_cselect_b32 s41, 1, 0
	v_cmp_lt_u32_e32 vcc, 0, v11
	s_and_saveexec_b64 s[22:23], vcc
	v_bfe_u32 v13, v68, 16, 8
	v_lshlrev_b32_e32 v13, 2, v13
	ds_add_rtn_u32 v80, v13, v12
	s_mov_b64 exec, s[22:23]
	v_cmp_lt_u32_e32 vcc, 1, v11
	s_and_saveexec_b64 s[22:23], vcc
	v_bfe_u32 v13, v69, 16, 8
	v_lshlrev_b32_e32 v13, 2, v13
	ds_add_rtn_u32 v81, v13, v12
	s_mov_b64 exec, s[22:23]
	v_cmp_lt_u32_e32 vcc, 2, v11
	s_and_saveexec_b64 s[22:23], vcc
	v_bfe_u32 v13, v70, 16, 8
	v_lshlrev_b32_e32 v13, 2, v13
	ds_add_rtn_u32 v82, v13, v12
	s_mov_b64 exec, s[22:23]
	v_cmp_lt_u32_e32 vcc, 3, v11
	s_and_saveexec_b64 s[22:23], vcc
	v_bfe_u32 v13, v71, 16, 8
	v_lshlrev_b32_e32 v13, 2, v13
	ds_add_rtn_u32 v83, v13, v12
	s_mov_b64 exec, s[22:23]
	s_cmp_eq_u32 s40, 0
	s_cbranch_scc1 .Lp2_c4_p1done
	v_cmp_lt_u32_e32 vcc, 4, v11
	s_and_saveexec_b64 s[22:23], vcc
	v_bfe_u32 v13, v72, 16, 8
	v_lshlrev_b32_e32 v13, 2, v13
	ds_add_rtn_u32 v84, v13, v12
	s_mov_b64 exec, s[22:23]
	v_cmp_lt_u32_e32 vcc, 5, v11
	s_and_saveexec_b64 s[22:23], vcc
	v_bfe_u32 v13, v73, 16, 8
	v_lshlrev_b32_e32 v13, 2, v13
	ds_add_rtn_u32 v85, v13, v12
	s_mov_b64 exec, s[22:23]
	v_cmp_lt_u32_e32 vcc, 6, v11
	s_and_saveexec_b64 s[22:23], vcc
	v_bfe_u32 v13, v74, 16, 8
	v_lshlrev_b32_e32 v13, 2, v13
	ds_add_rtn_u32 v86, v13, v12
	s_mov_b64 exec, s[22:23]
	v_cmp_lt_u32_e32 vcc, 7, v11
	s_and_saveexec_b64 s[22:23], vcc
	v_bfe_u32 v13, v75, 16, 8
	v_lshlrev_b32_e32 v13, 2, v13
	ds_add_rtn_u32 v87, v13, v12
	s_mov_b64 exec, s[22:23]
	s_cmp_eq_u32 s41, 0
	s_cbranch_scc1 .Lp2_c4_p1done
	v_cmp_lt_u32_e32 vcc, 8, v11
	s_and_saveexec_b64 s[22:23], vcc
	v_bfe_u32 v13, v76, 16, 8
	v_lshlrev_b32_e32 v13, 2, v13
	ds_add_rtn_u32 v88, v13, v12
	s_mov_b64 exec, s[22:23]
	v_cmp_lt_u32_e32 vcc, 9, v11
	s_and_saveexec_b64 s[22:23], vcc
	v_bfe_u32 v13, v77, 16, 8
	v_lshlrev_b32_e32 v13, 2, v13
	ds_add_rtn_u32 v89, v13, v12
	s_mov_b64 exec, s[22:23]
	v_cmp_lt_u32_e32 vcc, 10, v11
	s_and_saveexec_b64 s[22:23], vcc
	v_bfe_u32 v13, v78, 16, 8
	v_lshlrev_b32_e32 v13, 2, v13
	ds_add_rtn_u32 v90, v13, v12
	s_mov_b64 exec, s[22:23]
	v_cmp_lt_u32_e32 vcc, 11, v11
	s_and_saveexec_b64 s[22:23], vcc
	v_bfe_u32 v13, v79, 16, 8
	v_lshlrev_b32_e32 v13, 2, v13
	ds_add_rtn_u32 v91, v13, v12
	s_mov_b64 exec, s[22:23]
.Lp2_c4_p1done:
	s_waitcnt lgkmcnt(0)
	v_cmp_lt_u32_e32 vcc, 0, v11
	v_cmp_gt_u32_e64 s[28:29], 32, v80
	s_and_b64 s[28:29], s[28:29], vcc
	s_and_saveexec_b64 s[22:23], s[28:29]
	v_lshrrev_b32_e32 v13, 16, v68
	v_lshl_add_u32 v13, v13, 5, v80
	v_lshlrev_b32_e32 v13, 2, v13
	v_and_b32_e32 v14, 0xffff, v68
	global_store_dword v13, v14, s[6:7] nt
	s_mov_b64 exec, s[22:23]
	v_cmp_lt_u32_e32 vcc, 1, v11
	v_cmp_gt_u32_e64 s[28:29], 32, v81
	s_and_b64 s[28:29], s[28:29], vcc
	s_and_saveexec_b64 s[22:23], s[28:29]
	v_lshrrev_b32_e32 v13, 16, v69
	v_lshl_add_u32 v13, v13, 5, v81
	v_lshlrev_b32_e32 v13, 2, v13
	v_and_b32_e32 v14, 0xffff, v69
	global_store_dword v13, v14, s[6:7] nt
	s_mov_b64 exec, s[22:23]
	v_cmp_lt_u32_e32 vcc, 2, v11
	v_cmp_gt_u32_e64 s[28:29], 32, v82
	s_and_b64 s[28:29], s[28:29], vcc
	s_and_saveexec_b64 s[22:23], s[28:29]
	v_lshrrev_b32_e32 v13, 16, v70
	v_lshl_add_u32 v13, v13, 5, v82
	v_lshlrev_b32_e32 v13, 2, v13
	v_and_b32_e32 v14, 0xffff, v70
	global_store_dword v13, v14, s[6:7] nt
	s_mov_b64 exec, s[22:23]
	v_cmp_lt_u32_e32 vcc, 3, v11
	v_cmp_gt_u32_e64 s[28:29], 32, v83
	s_and_b64 s[28:29], s[28:29], vcc
	s_and_saveexec_b64 s[22:23], s[28:29]
	v_lshrrev_b32_e32 v13, 16, v71
	v_lshl_add_u32 v13, v13, 5, v83
	v_lshlrev_b32_e32 v13, 2, v13
	v_and_b32_e32 v14, 0xffff, v71
	global_store_dword v13, v14, s[6:7] nt
	s_mov_b64 exec, s[22:23]
	s_cmp_eq_u32 s40, 0
	s_cbranch_scc1 .Lp2_c4_p2done
	v_cmp_lt_u32_e32 vcc, 4, v11
	v_cmp_gt_u32_e64 s[28:29], 32, v84
	s_and_b64 s[28:29], s[28:29], vcc
	s_and_saveexec_b64 s[22:23], s[28:29]
	v_lshrrev_b32_e32 v13, 16, v72
	v_lshl_add_u32 v13, v13, 5, v84
	v_lshlrev_b32_e32 v13, 2, v13
	v_and_b32_e32 v14, 0xffff, v72
	global_store_dword v13, v14, s[6:7] nt
	s_mov_b64 exec, s[22:23]
	v_cmp_lt_u32_e32 vcc, 5, v11
	v_cmp_gt_u32_e64 s[28:29], 32, v85
	s_and_b64 s[28:29], s[28:29], vcc
	s_and_saveexec_b64 s[22:23], s[28:29]
	v_lshrrev_b32_e32 v13, 16, v73
	v_lshl_add_u32 v13, v13, 5, v85
	v_lshlrev_b32_e32 v13, 2, v13
	v_and_b32_e32 v14, 0xffff, v73
	global_store_dword v13, v14, s[6:7] nt
	s_mov_b64 exec, s[22:23]
	v_cmp_lt_u32_e32 vcc, 6, v11
	v_cmp_gt_u32_e64 s[28:29], 32, v86
	s_and_b64 s[28:29], s[28:29], vcc
	s_and_saveexec_b64 s[22:23], s[28:29]
	v_lshrrev_b32_e32 v13, 16, v74
	v_lshl_add_u32 v13, v13, 5, v86
	v_lshlrev_b32_e32 v13, 2, v13
	v_and_b32_e32 v14, 0xffff, v74
	global_store_dword v13, v14, s[6:7] nt
	s_mov_b64 exec, s[22:23]
	v_cmp_lt_u32_e32 vcc, 7, v11
	v_cmp_gt_u32_e64 s[28:29], 32, v87
	s_and_b64 s[28:29], s[28:29], vcc
	s_and_saveexec_b64 s[22:23], s[28:29]
	v_lshrrev_b32_e32 v13, 16, v75
	v_lshl_add_u32 v13, v13, 5, v87
	v_lshlrev_b32_e32 v13, 2, v13
	v_and_b32_e32 v14, 0xffff, v75
	global_store_dword v13, v14, s[6:7] nt
	s_mov_b64 exec, s[22:23]
	s_cmp_eq_u32 s41, 0
	s_cbranch_scc1 .Lp2_c4_p2done
	v_cmp_lt_u32_e32 vcc, 8, v11
	v_cmp_gt_u32_e64 s[28:29], 32, v88
	s_and_b64 s[28:29], s[28:29], vcc
	s_and_saveexec_b64 s[22:23], s[28:29]
	v_lshrrev_b32_e32 v13, 16, v76
	v_lshl_add_u32 v13, v13, 5, v88
	v_lshlrev_b32_e32 v13, 2, v13
	v_and_b32_e32 v14, 0xffff, v76
	global_store_dword v13, v14, s[6:7] nt
	s_mov_b64 exec, s[22:23]
	v_cmp_lt_u32_e32 vcc, 9, v11
	v_cmp_gt_u32_e64 s[28:29], 32, v89
	s_and_b64 s[28:29], s[28:29], vcc
	s_and_saveexec_b64 s[22:23], s[28:29]
	v_lshrrev_b32_e32 v13, 16, v77
	v_lshl_add_u32 v13, v13, 5, v89
	v_lshlrev_b32_e32 v13, 2, v13
	v_and_b32_e32 v14, 0xffff, v77
	global_store_dword v13, v14, s[6:7] nt
	s_mov_b64 exec, s[22:23]
	v_cmp_lt_u32_e32 vcc, 10, v11
	v_cmp_gt_u32_e64 s[28:29], 32, v90
	s_and_b64 s[28:29], s[28:29], vcc
	s_and_saveexec_b64 s[22:23], s[28:29]
	v_lshrrev_b32_e32 v13, 16, v78
	v_lshl_add_u32 v13, v13, 5, v90
	v_lshlrev_b32_e32 v13, 2, v13
	v_and_b32_e32 v14, 0xffff, v78
	global_store_dword v13, v14, s[6:7] nt
	s_mov_b64 exec, s[22:23]
	v_cmp_lt_u32_e32 vcc, 11, v11
	v_cmp_gt_u32_e64 s[28:29], 32, v91
	s_and_b64 s[28:29], s[28:29], vcc
	s_and_saveexec_b64 s[22:23], s[28:29]
	v_lshrrev_b32_e32 v13, 16, v79
	v_lshl_add_u32 v13, v13, 5, v91
	v_lshlrev_b32_e32 v13, 2, v13
	v_and_b32_e32 v14, 0xffff, v79
	global_store_dword v13, v14, s[6:7] nt
	s_mov_b64 exec, s[22:23]
.Lp2_c4_p2done:
	v_cmp_lt_u32_e64 s[28:29], 12, v11
	s_cmp_eq_u64 s[28:29], 0
	s_cbranch_scc1 .Lp2_c4_taildone
	v_mov_b32_e32 v15, 12
.Lp2_c4_tail:
	v_cmp_lt_u32_e32 vcc, v15, v11
	s_and_saveexec_b64 s[22:23], vcc
	s_cbranch_execz .Lp2_c4_tailend
	v_lshl_add_u32 v13, v15, 2, v6
	global_load_dword v16, v13, s[26:27] sc1
	s_waitcnt vmcnt(0)
	v_bfe_u32 v13, v16, 16, 8
	v_lshlrev_b32_e32 v13, 2, v13
	ds_add_rtn_u32 v17, v13, v12
	s_waitcnt lgkmcnt(0)
	v_cmp_gt_u32_e32 vcc, 32, v17
	s_and_b64 exec, exec, vcc
	v_lshrrev_b32_e32 v13, 16, v16
	v_lshl_add_u32 v13, v13, 5, v17
	v_lshlrev_b32_e32 v13, 2, v13
	v_and_b32_e32 v14, 0xffff, v16
	global_store_dword v13, v14, s[6:7] nt
	s_mov_b64 exec, s[22:23]
	v_add_u32_e32 v15, 1, v15
	s_branch .Lp2_c4_tail

.Lp2_c4_taildone:
	s_waitcnt vmcnt(0) lgkmcnt(0)
	s_barrier
	v_lshlrev_b32_e32 v13, 2, v0
	ds_read_b32 v14, v13
	ds_read_b32 v15, v13 offset:512
	s_lshl_b32 s3, s33, 8
	v_add_u32_e32 v16, s3, v0
	v_add_u32_e32 v17, 0x80, v16
	v_lshlrev_b32_e32 v13, 2, v16
	s_waitcnt lgkmcnt(0)
	v_cmp_gt_u32_e32 vcc, s30, v16
	s_and_saveexec_b64 s[22:23], vcc
	global_store_dword v13, v14, s[4:5]
	s_mov_b64 exec, s[22:23]
	v_cmp_gt_u32_e32 vcc, s30, v17
	s_and_saveexec_b64 s[22:23], vcc
	global_store_dword v13, v15, s[4:5] offset:512
	s_mov_b64 exec, s[22:23]
	v_max_u32_e32 v18, v14, v15
	v_cmp_lt_u32_e64 s[28:29], 32, v18
	s_cmp_eq_u64 s[28:29], 0
	s_cbranch_scc1 .Lp2_noflag
	ds_write_b32 v19, v12 offset:1028
.Lp2_noflag:
	s_waitcnt lgkmcnt(0)
	s_barrier
	ds_read_b32 v18, v19 offset:1028
	s_waitcnt lgkmcnt(0)
	v_readfirstlane_b32 s3, v18
	s_cmp_eq_u32 s3, 0
	s_cbranch_scc1 .Lp2_end
	s_waitcnt vmcnt(0)
	v_mov_b32_e32 v15, 0
.Lp2_s0_loop:
	v_cmp_lt_u32_e32 vcc, v15, v7
	s_and_saveexec_b64 s[22:23], vcc
	s_cbranch_execz .Lp2_s0_end
	v_lshl_add_u32 v13, v15, 2, v2
	global_load_dword v16, v13, s[26:27] sc1
	s_waitcnt vmcnt(0)
	v_bfe_u32 v13, v16, 16, 8
	v_lshlrev_b32_e32 v13, 2, v13
	ds_read_b32 v17, v13
	s_waitcnt lgkmcnt(0)
	v_cmp_lt_u32_e32 vcc, 32, v17
	s_and_b64 exec, exec, vcc
	s_cbranch_execz .Lp2_s0_next
	ds_add_rtn_u32 v17, v13, v12 offset:2048
	v_lshrrev_b32_e32 v18, 16, v16
	v_and_b32_e32 v14, 0xffff, v16
	s_waitcnt lgkmcnt(0)
	s_mov_b64 s[28:29], exec
	v_cmp_gt_u32_e32 vcc, 32, v17
	s_and_b64 exec, s[28:29], vcc
	v_lshl_add_u32 v13, v18, 5, v17
	v_lshlrev_b32_e32 v13, 2, v13
	global_store_dword v13, v14, s[6:7]
	s_andn2_b64 exec, s[28:29], vcc
	s_cbranch_execz .Lp2_s0_next
	global_atomic_add v13, v19, v12, s[10:11] sc0
	s_waitcnt vmcnt(0)
	v_lshlrev_b32_e32 v13, 2, v13
	global_store_dword v13, v18, s[16:17]
	global_store_dword v13, v14, s[18:19]
	v_cmp_eq_u32_e32 vcc, 32, v17
	s_and_b64 exec, exec, vcc
	s_cbranch_execz .Lp2_s0_next
	global_atomic_add v13, v19, v12, s[10:11] offset:4 sc0
	s_waitcnt vmcnt(0)
	v_lshlrev_b32_e32 v13, 2, v13
	global_store_dword v13, v18, s[20:21]
.Lp2_s0_next:
	s_mov_b64 exec, s[22:23]
	v_add_u32_e32 v15, 1, v15
	s_branch .Lp2_s0_loop
.Lp2_s0_end:
	s_mov_b64 exec, s[22:23]
	v_mov_b32_e32 v15, 0
.Lp2_s1_loop:
	v_cmp_lt_u32_e32 vcc, v15, v8
	s_and_saveexec_b64 s[22:23], vcc
	s_cbranch_execz .Lp2_s1_end
	v_lshl_add_u32 v13, v15, 2, v3
	global_load_dword v16, v13, s[26:27] sc1
	s_waitcnt vmcnt(0)
	v_bfe_u32 v13, v16, 16, 8
	v_lshlrev_b32_e32 v13, 2, v13
	ds_read_b32 v17, v13
	s_waitcnt lgkmcnt(0)
	v_cmp_lt_u32_e32 vcc, 32, v17
	s_and_b64 exec, exec, vcc
	s_cbranch_execz .Lp2_s1_next
	ds_add_rtn_u32 v17, v13, v12 offset:2048
	v_lshrrev_b32_e32 v18, 16, v16
	v_and_b32_e32 v14, 0xffff, v16
	s_waitcnt lgkmcnt(0)
	s_mov_b64 s[28:29], exec
	v_cmp_gt_u32_e32 vcc, 32, v17
	s_and_b64 exec, s[28:29], vcc
	v_lshl_add_u32 v13, v18, 5, v17
	v_lshlrev_b32_e32 v13, 2, v13
	global_store_dword v13, v14, s[6:7]
	s_andn2_b64 exec, s[28:29], vcc
	s_cbranch_execz .Lp2_s1_next
	global_atomic_add v13, v19, v12, s[10:11] sc0
	s_waitcnt vmcnt(0)
	v_lshlrev_b32_e32 v13, 2, v13
	global_store_dword v13, v18, s[16:17]
	global_store_dword v13, v14, s[18:19]
	v_cmp_eq_u32_e32 vcc, 32, v17
	s_and_b64 exec, exec, vcc
	s_cbranch_execz .Lp2_s1_next
	global_atomic_add v13, v19, v12, s[10:11] offset:4 sc0
	s_waitcnt vmcnt(0)
	v_lshlrev_b32_e32 v13, 2, v13
	global_store_dword v13, v18, s[20:21]

.Lp2_s2_loop:
	v_cmp_lt_u32_e32 vcc, v15, v9
	s_and_saveexec_b64 s[22:23], vcc
	s_cbranch_execz .Lp2_s2_end
	v_lshl_add_u32 v13, v15, 2, v4
	global_load_dword v16, v13, s[26:27] sc1
	s_waitcnt vmcnt(0)
	v_bfe_u32 v13, v16, 16, 8
	v_lshlrev_b32_e32 v13, 2, v13
	ds_read_b32 v17, v13
	s_waitcnt lgkmcnt(0)
	v_cmp_lt_u32_e32 vcc, 32, v17
	s_and_b64 exec, exec, vcc
	s_cbranch_execz .Lp2_s2_next
	ds_add_rtn_u32 v17, v13, v12 offset:2048
	v_lshrrev_b32_e32 v18, 16, v16
	v_and_b32_e32 v14, 0xffff, v16
	s_waitcnt lgkmcnt(0)
	s_mov_b64 s[28:29], exec
	v_cmp_gt_u32_e32 vcc, 32, v17
	s_and_b64 exec, s[28:29], vcc
	v_lshl_add_u32 v13, v18, 5, v17
	v_lshlrev_b32_e32 v13, 2, v13
	global_store_dword v13, v14, s[6:7]
	s_andn2_b64 exec, s[28:29], vcc
	s_cbranch_execz .Lp2_s2_next
	global_atomic_add v13, v19, v12, s[10:11] sc0
	s_waitcnt vmcnt(0)
	v_lshlrev_b32_e32 v13, 2, v13
	global_store_dword v13, v18, s[16:17]
	global_store_dword v13, v14, s[18:19]
	v_cmp_eq_u32_e32 vcc, 32, v17
	s_and_b64 exec, exec, vcc
	s_cbranch_execz .Lp2_s2_next
	global_atomic_add v13, v19, v12, s[10:11] offset:4 sc0
	s_waitcnt vmcnt(0)
	v_lshlrev_b32_e32 v13, 2, v13
	global_store_dword v13, v18, s[20:21]

.Lp2_s3_loop:
	v_cmp_lt_u32_e32 vcc, v15, v10
	s_and_saveexec_b64 s[22:23], vcc
	s_cbranch_execz .Lp2_s3_end
	v_lshl_add_u32 v13, v15, 2, v5
	global_load_dword v16, v13, s[26:27] sc1
	s_waitcnt vmcnt(0)
	v_bfe_u32 v13, v16, 16, 8
	v_lshlrev_b32_e32 v13, 2, v13
	ds_read_b32 v17, v13
	s_waitcnt lgkmcnt(0)
	v_cmp_lt_u32_e32 vcc, 32, v17
	s_and_b64 exec, exec, vcc
	s_cbranch_execz .Lp2_s3_next
	ds_add_rtn_u32 v17, v13, v12 offset:2048
	v_lshrrev_b32_e32 v18, 16, v16
	v_and_b32_e32 v14, 0xffff, v16
	s_waitcnt lgkmcnt(0)
	s_mov_b64 s[28:29], exec
	v_cmp_gt_u32_e32 vcc, 32, v17
	s_and_b64 exec, s[28:29], vcc
	v_lshl_add_u32 v13, v18, 5, v17
	v_lshlrev_b32_e32 v13, 2, v13
	global_store_dword v13, v14, s[6:7]
	s_andn2_b64 exec, s[28:29], vcc
	s_cbranch_execz .Lp2_s3_next
	global_atomic_add v13, v19, v12, s[10:11] sc0
	s_waitcnt vmcnt(0)
	v_lshlrev_b32_e32 v13, 2, v13
	global_store_dword v13, v18, s[16:17]
	global_store_dword v13, v14, s[18:19]
	v_cmp_eq_u32_e32 vcc, 32, v17
	s_and_b64 exec, exec, vcc
	s_cbranch_execz .Lp2_s3_next
	global_atomic_add v13, v19, v12, s[10:11] offset:4 sc0
	s_waitcnt vmcnt(0)
	v_lshlrev_b32_e32 v13, 2, v13
	global_store_dword v13, v18, s[20:21]

.Lp2_s4_loop:
	v_cmp_lt_u32_e32 vcc, v15, v11
	s_and_saveexec_b64 s[22:23], vcc
	s_cbranch_execz .Lp2_s4_end
	v_lshl_add_u32 v13, v15, 2, v6
	global_load_dword v16, v13, s[26:27] sc1
	s_waitcnt vmcnt(0)
	v_bfe_u32 v13, v16, 16, 8
	v_lshlrev_b32_e32 v13, 2, v13
	ds_read_b32 v17, v13
	s_waitcnt lgkmcnt(0)
	v_cmp_lt_u32_e32 vcc, 32, v17
	s_and_b64 exec, exec, vcc
	s_cbranch_execz .Lp2_s4_next
	ds_add_rtn_u32 v17, v13, v12 offset:2048
	v_lshrrev_b32_e32 v18, 16, v16
	v_and_b32_e32 v14, 0xffff, v16
	s_waitcnt lgkmcnt(0)
	s_mov_b64 s[28:29], exec
	v_cmp_gt_u32_e32 vcc, 32, v17
	s_and_b64 exec, s[28:29], vcc
	v_lshl_add_u32 v13, v18, 5, v17
	v_lshlrev_b32_e32 v13, 2, v13
	global_store_dword v13, v14, s[6:7]
	s_andn2_b64 exec, s[28:29], vcc
	s_cbranch_execz .Lp2_s4_next
	global_atomic_add v13, v19, v12, s[10:11] sc0
	s_waitcnt vmcnt(0)
	v_lshlrev_b32_e32 v13, 2, v13
	global_store_dword v13, v18, s[16:17]
	global_store_dword v13, v14, s[18:19]
	v_cmp_eq_u32_e32 vcc, 32, v17
	s_and_b64 exec, exec, vcc
	s_cbranch_execz .Lp2_s4_next
	global_atomic_add v13, v19, v12, s[10:11] offset:4 sc0
	s_waitcnt vmcnt(0)
	v_lshlrev_b32_e32 v13, 2, v13
	global_store_dword v13, v18, s[20:21]

	.amdhsa_kernel _Z6k_prepPKiS0_PiS1_S1_S1_S1_S1_S1_PKfPKDF16_PDF16_Pf
		.amdhsa_group_segment_fixed_size 8200
		.amdhsa_private_segment_fixed_size 0
		.amdhsa_kernarg_size 104
		.amdhsa_user_sgpr_count 2
		.amdhsa_user_sgpr_dispatch_ptr 0
		.amdhsa_user_sgpr_queue_ptr 0
		.amdhsa_user_sgpr_kernarg_segment_ptr 1
		.amdhsa_user_sgpr_dispatch_id 0
		.amdhsa_user_sgpr_kernarg_preload_length 0
		.amdhsa_user_sgpr_kernarg_preload_offset 0
		.amdhsa_user_sgpr_private_segment_size 0
		.amdhsa_uses_dynamic_stack 0
		.amdhsa_enable_private_segment 0
		.amdhsa_system_sgpr_workgroup_id_x 1
		.amdhsa_system_sgpr_workgroup_id_y 0
		.amdhsa_system_sgpr_workgroup_id_z 0
		.amdhsa_system_sgpr_workgroup_info 0
		.amdhsa_system_vgpr_workitem_id 0
		.amdhsa_next_free_vgpr 96
		.amdhsa_next_free_sgpr 48
		.amdhsa_accum_offset 92
		.amdhsa_reserve_vcc 1
		.amdhsa_float_round_mode_32 0
		.amdhsa_float_round_mode_16_64 0
		.amdhsa_float_denorm_mode_32 3
		.amdhsa_float_denorm_mode_16_64 3
		.amdhsa_dx10_clamp 1
		.amdhsa_ieee_mode 1
		.amdhsa_fp16_overflow 0
		.amdhsa_tg_split 0
		.amdhsa_exception_fp_ieee_invalid_op 0
		.amdhsa_exception_fp_denorm_src 0
		.amdhsa_exception_fp_ieee_div_zero 0
		.amdhsa_exception_fp_ieee_overflow 0
		.amdhsa_exception_fp_ieee_underflow 0
		.amdhsa_exception_fp_ieee_inexact 0
		.amdhsa_exception_int_div_zero 0
	.end_amdhsa_kernel

amdhsa.kernels:
  - .agpr_count:     0
    .args:
      - .actual_access:  read_only
        .address_space:  global
        .offset:         0
        .size:           8
        .value_kind:     global_buffer
      - .actual_access:  read_only
        .address_space:  global
        .offset:         8
        .size:           8
        .value_kind:     global_buffer
      - .actual_access:  read_only
        .address_space:  global
        .offset:         16
        .size:           8
        .value_kind:     global_buffer
      - .actual_access:  read_only
        .address_space:  global
        .offset:         24
        .size:           8
        .value_kind:     global_buffer
      - .actual_access:  write_only
        .address_space:  global
        .offset:         32
        .size:           8
        .value_kind:     global_buffer
      - .actual_access:  write_only
        .address_space:  global
        .offset:         40
        .size:           8
        .value_kind:     global_buffer
      - .actual_access:  write_only
        .address_space:  global
        .offset:         48
        .size:           8
        .value_kind:     global_buffer
      - .actual_access:  write_only
        .address_space:  global
        .offset:         56
        .size:           8
        .value_kind:     global_buffer
      - .actual_access:  write_only
        .address_space:  global
        .offset:         64
        .size:           8
        .value_kind:     global_buffer
      - .offset:         72
        .size:           4
        .value_kind:     by_value
      - .offset:         80
        .size:           4
        .value_kind:     hidden_block_count_x
      - .offset:         84
        .size:           4
        .value_kind:     hidden_block_count_y
      - .offset:         88
        .size:           4
        .value_kind:     hidden_block_count_z
      - .offset:         92
        .size:           2
        .value_kind:     hidden_group_size_x
      - .offset:         94
        .size:           2
        .value_kind:     hidden_group_size_y
      - .offset:         96
        .size:           2
        .value_kind:     hidden_group_size_z
      - .offset:         98
        .size:           2
        .value_kind:     hidden_remainder_x
      - .offset:         100
        .size:           2
        .value_kind:     hidden_remainder_y
      - .offset:         102
        .size:           2
        .value_kind:     hidden_remainder_z
      - .offset:         120
        .size:           8
        .value_kind:     hidden_global_offset_x
      - .offset:         128
        .size:           8
        .value_kind:     hidden_global_offset_y
      - .offset:         136
        .size:           8
        .value_kind:     hidden_global_offset_z
      - .offset:         144
        .size:           2
        .value_kind:     hidden_grid_dims
    .group_segment_fixed_size: 0
    .kernarg_segment_align: 8
    .kernarg_segment_size: 336
    .language:       OpenCL C
    .language_version:
      - 2
      - 0
    .max_flat_workgroup_size: 256
    .name:           _Z7k_prepwPKfS0_S0_S0_PfPDF16_S2_S2_Pii
    .private_segment_fixed_size: 0
    .sgpr_count:     30
    .sgpr_spill_count: 0
    .symbol:         _Z7k_prepwPKfS0_S0_S0_PfPDF16_S2_S2_Pii.kd
    .uniform_work_group_size: 1
    .uses_dynamic_stack: false
    .vgpr_count:     66
    .vgpr_spill_count: 0
    .wavefront_size: 64
  - .agpr_count:     4
    .args:
      - .actual_access:  read_only
        .address_space:  global
        .offset:         0
        .size:           8
        .value_kind:     global_buffer
      - .actual_access:  read_only
        .address_space:  global
        .offset:         8
        .size:           8
        .value_kind:     global_buffer
      - .address_space:  global
        .offset:         16
        .size:           8
        .value_kind:     global_buffer
      - .actual_access:  write_only
        .address_space:  global
        .offset:         24
        .size:           8
        .value_kind:     global_buffer
      - .address_space:  global
        .offset:         32
        .size:           8
        .value_kind:     global_buffer
      - .address_space:  global
        .offset:         40
        .size:           8
        .value_kind:     global_buffer
      - .actual_access:  write_only
        .address_space:  global
        .offset:         48
        .size:           8
        .value_kind:     global_buffer
      - .actual_access:  write_only
        .address_space:  global
        .offset:         56
        .size:           8
        .value_kind:     global_buffer
      - .actual_access:  write_only
        .address_space:  global
        .offset:         64
        .size:           8
        .value_kind:     global_buffer
      - .actual_access:  read_only
        .address_space:  global
        .offset:         72
        .size:           8
        .value_kind:     global_buffer
      - .actual_access:  read_only
        .address_space:  global
        .offset:         80
        .size:           8
        .value_kind:     global_buffer
      - .actual_access:  write_only
        .address_space:  global
        .offset:         88
        .size:           8
        .value_kind:     global_buffer
      - .actual_access:  write_only
        .address_space:  global
        .offset:         96
        .size:           8
        .value_kind:     global_buffer
    .group_segment_fixed_size: 8200
    .kernarg_segment_align: 8
    .kernarg_segment_size: 104
    .language:       OpenCL C
    .language_version:
      - 2
      - 0
    .max_flat_workgroup_size: 128
    .name:           _Z6k_prepPKiS0_PiS1_S1_S1_S1_S1_S1_PKfPKDF16_PDF16_Pf
    .private_segment_fixed_size: 0
    .sgpr_count:     54
    .sgpr_spill_count: 0
    .symbol:         _Z6k_prepPKiS0_PiS1_S1_S1_S1_S1_S1_PKfPKDF16_PDF16_Pf.kd
    .uniform_work_group_size: 1
    .uses_dynamic_stack: false
    .vgpr_count:     96
    .vgpr_spill_count: 0
    .wavefront_size: 64
  - .agpr_count:     0
    .args:
      - .actual_access:  read_only
        .address_space:  global
        .offset:         0
        .size:           8
        .value_kind:     global_buffer
      - .actual_access:  read_only
        .address_space:  global
        .offset:         8
        .size:           8
        .value_kind:     global_buffer
      - .actual_access:  read_only
        .address_space:  global
        .offset:         16
        .size:           8
        .value_kind:     global_buffer
      - .actual_access:  read_only
        .address_space:  global
        .offset:         24
        .size:           8
        .value_kind:     global_buffer
      - .actual_access:  read_only
        .address_space:  global
        .offset:         32
        .size:           8
        .value_kind:     global_buffer
      - .actual_access:  read_only
        .address_space:  global
        .offset:         40
        .size:           8
        .value_kind:     global_buffer
      - .actual_access:  read_only
        .address_space:  global
        .offset:         48
        .size:           8
        .value_kind:     global_buffer
      - .actual_access:  read_only
        .address_space:  global
        .offset:         56
        .size:           8
        .value_kind:     global_buffer
      - .actual_access:  read_only
        .address_space:  global
        .offset:         64
        .size:           8
        .value_kind:     global_buffer
      - .actual_access:  read_only
        .address_space:  global
        .offset:         72
        .size:           8
        .value_kind:     global_buffer
      - .actual_access:  read_only
        .address_space:  global
        .offset:         80
        .size:           8
        .value_kind:     global_buffer
      - .actual_access:  read_only
        .address_space:  global
        .offset:         88
        .size:           8
        .value_kind:     global_buffer
      - .actual_access:  read_only
        .address_space:  global
        .offset:         96
        .size:           8
        .value_kind:     global_buffer
      - .actual_access:  read_only
        .address_space:  global
        .offset:         104
        .size:           8
        .value_kind:     global_buffer
      - .actual_access:  read_only
        .address_space:  global
        .offset:         112
        .size:           8
        .value_kind:     global_buffer
      - .actual_access:  read_only
        .address_space:  global
        .offset:         120
        .size:           8
        .value_kind:     global_buffer
      - .actual_access:  write_only
        .address_space:  global
        .offset:         128
        .size:           8
        .value_kind:     global_buffer
      - .actual_access:  write_only
        .address_space:  global
        .offset:         136
        .size:           8
        .value_kind:     global_buffer
    .group_segment_fixed_size: 81920
    .kernarg_segment_align: 8
    .kernarg_segment_size: 144
    .language:       OpenCL C
    .language_version:
      - 2
      - 0
    .max_flat_workgroup_size: 512
    .name:           _Z4k_l1PKDF16_PKfPKiS4_S4_S4_S4_S4_S4_S2_S2_S0_S0_S2_S2_S2_PDF16_Pf
    .private_segment_fixed_size: 0
    .sgpr_count:     57
    .sgpr_spill_count: 0
    .symbol:         _Z4k_l1PKDF16_PKfPKiS4_S4_S4_S4_S4_S4_S2_S2_S0_S0_S2_S2_S2_PDF16_Pf.kd
    .uniform_work_group_size: 1
    .uses_dynamic_stack: false
    .vgpr_count:     128
    .vgpr_spill_count: 0
    .wavefront_size: 64
  - .agpr_count:     0
    .args:
      - .actual_access:  read_only
        .address_space:  global
        .offset:         0
        .size:           8
        .value_kind:     global_buffer
      - .actual_access:  read_only
        .address_space:  global
        .offset:         8
        .size:           8
        .value_kind:     global_buffer
      - .actual_access:  read_only
        .address_space:  global
        .offset:         16
        .size:           8
        .value_kind:     global_buffer
      - .actual_access:  read_only
        .address_space:  global
        .offset:         24
        .size:           8
        .value_kind:     global_buffer
      - .actual_access:  read_only
        .address_space:  global
        .offset:         32
        .size:           8
        .value_kind:     global_buffer
      - .actual_access:  read_only
        .address_space:  global
        .offset:         40
        .size:           8
        .value_kind:     global_buffer
      - .actual_access:  read_only
        .address_space:  global
        .offset:         48
        .size:           8
        .value_kind:     global_buffer
      - .actual_access:  read_only
        .address_space:  global
        .offset:         56
        .size:           8
        .value_kind:     global_buffer
      - .actual_access:  read_only
        .address_space:  global
        .offset:         64
        .size:           8
        .value_kind:     global_buffer
      - .actual_access:  read_only
        .address_space:  global
        .offset:         72
        .size:           8
        .value_kind:     global_buffer
      - .actual_access:  read_only
        .address_space:  global
        .offset:         80
        .size:           8
        .value_kind:     global_buffer
      - .actual_access:  read_only
        .address_space:  global
        .offset:         88
        .size:           8
        .value_kind:     global_buffer
      - .address_space:  global
        .offset:         96
        .size:           8
        .value_kind:     global_buffer
      - .address_space:  global
        .offset:         104
        .size:           8
        .value_kind:     global_buffer
      - .offset:         112
        .size:           4
        .value_kind:     hidden_block_count_x
      - .offset:         116
        .size:           4
        .value_kind:     hidden_block_count_y
      - .offset:         120
        .size:           4
        .value_kind:     hidden_block_count_z
      - .offset:         124
        .size:           2
        .value_kind:     hidden_group_size_x
      - .offset:         126
        .size:           2
        .value_kind:     hidden_group_size_y
      - .offset:         128
        .size:           2
        .value_kind:     hidden_group_size_z
      - .offset:         130
        .size:           2
        .value_kind:     hidden_remainder_x
      - .offset:         132
        .size:           2
        .value_kind:     hidden_remainder_y
      - .offset:         134
        .size:           2
        .value_kind:     hidden_remainder_z
      - .offset:         152
        .size:           8
        .value_kind:     hidden_global_offset_x
      - .offset:         160
        .size:           8
        .value_kind:     hidden_global_offset_y
      - .offset:         168
        .size:           8
        .value_kind:     hidden_global_offset_z
      - .offset:         176
        .size:           2
        .value_kind:     hidden_grid_dims
    .group_segment_fixed_size: 4160
    .kernarg_segment_align: 8
    .kernarg_segment_size: 368
    .language:       OpenCL C
    .language_version:
      - 2
      - 0
    .max_flat_workgroup_size: 256
    .name:           _Z4k_l2PKDF16_PKfPKiS4_S4_S4_S4_S4_S4_S2_S2_S2_PfPi
    .private_segment_fixed_size: 0
    .sgpr_count:     54
    .sgpr_spill_count: 0
    .symbol:         _Z4k_l2PKDF16_PKfPKiS4_S4_S4_S4_S4_S4_S2_S2_S2_PfPi.kd
    .uniform_work_group_size: 1
    .uses_dynamic_stack: false
    .vgpr_count:     118
    .vgpr_spill_count: 0
    .wavefront_size: 64
  - .agpr_count:     0
    .args:
      - .actual_access:  read_only
        .address_space:  global
        .offset:         0
        .size:           8
        .value_kind:     global_buffer
      - .actual_access:  read_only
        .address_space:  global
        .offset:         8
        .size:           8
        .value_kind:     global_buffer
      - .actual_access:  read_only
        .address_space:  global
        .offset:         16
        .size:           8
        .value_kind:     global_buffer
      - .actual_access:  read_only
        .address_space:  global
        .offset:         24
        .size:           8
        .value_kind:     global_buffer
      - .actual_access:  write_only
        .address_space:  global
        .offset:         32
        .size:           8
        .value_kind:     global_buffer
    .group_segment_fixed_size: 6208
    .kernarg_segment_align: 8
    .kernarg_segment_size: 40
    .language:       OpenCL C
    .language_version:
      - 2
      - 0
    .max_flat_workgroup_size: 1024
    .name:           _Z7k_finalPKfPKiS0_S0_Pf
    .private_segment_fixed_size: 0
    .sgpr_count:     16
    .sgpr_spill_count: 0
    .symbol:         _Z7k_finalPKfPKiS0_S0_Pf.kd
    .uniform_work_group_size: 1
    .uses_dynamic_stack: false
    .vgpr_count:     38
    .vgpr_spill_count: 0
    .wavefront_size: 64
